# baseline (speedup 1.0000x reference)
_Z9proj_gemmPKfS0_S0_PK14__hip_bfloat16S0_S0_S0_PS1_:
	v_readfirstlane_b32 s40, v0
	s_nop 3
	s_lshr_b32 s40, s40, 8
	s_lshl_b32 s3, s2, 2
	s_load_dwordx8 s[8:15], s[0:1], 0x0
	s_and_b32 s3, s3, 28
	s_bfe_u32 s30, s2, 0x20005
	s_lshr_b32 s6, s2, 3
	s_ashr_i32 s18, s2, 7
	s_lshr_b32 s7, s2, 5
	s_or_b32 s20, s3, s30
	s_bfe_u32 s3, s2, 0x20003
	s_cmpk_lt_u32 s2, 0x80
	s_cselect_b64 s[16:17], -1, 0
	s_and_b64 s[4:5], s[16:17], exec
	s_waitcnt lgkmcnt(0)
	s_cselect_b32 s4, s9, s11
	s_cselect_b32 s5, s8, s10
	s_lshl_b32 s24, s20, 18
	s_lshl_b32 s8, s20, 20
	s_add_u32 s25, s5, s8
	s_addc_u32 s26, s4, 0
	s_ashr_i32 s19, s18, 31
	s_lshl_b64 s[4:5], s[18:19], 21
	s_add_u32 s4, s14, s4
	s_addc_u32 s5, s15, s5
	s_lshl_b32 s8, s3, 19
	s_add_u32 s27, s4, s8
	s_addc_u32 s28, s5, 0
	s_xor_b32 s6, s6, s18
	v_lshlrev_b32_e32 v1, 4, v0
	s_lshl_b32 s34, s6, 4
	v_lshlrev_b32_e32 v2, 3, v0
	v_and_b32_e32 v3, 0x1f0, v1
	s_movk_i32 s6, 0x200
	s_lshl_b32 s4, s20, 1
	s_mul_i32 s31, s18, 5
	s_xor_b32 s7, s7, s18
	v_lshrrev_b32_e32 v28, 6, v0
	s_and_b32 s35, s34, 16
	v_and_or_b32 v29, v2, s6, v3
	v_lshrrev_b32_e32 v2, 1, v0
	v_and_b32_e32 v3, 48, v1
	s_add_i32 s4, s4, s31
	v_bitop3_b32 v2, v2, v3, 32 bitop3:0x6c
	v_or_b32_e32 v30, s35, v28
	s_lshl_b32 s38, s7, 4
	s_and_b32 s5, s4, 15
	v_lshrrev_b32_e32 v2, 1, v2
	v_or_b32_e32 v32, 8, v30
	s_and_b32 s39, s38, 16
	v_and_or_b32 v178, v0, 32, v2
	v_lshlrev_b32_e32 v2, 3, v30
	v_lshrrev_b32_e32 v31, 6, v29
	s_movk_i32 s36, 0xb0
	v_lshlrev_b32_e32 v3, 3, v32
	s_movk_i32 s37, 0xf0
	v_or_b32_e32 v33, s39, v28
	s_lshl_b32 s33, s4, 6
	s_lshl_b32 s4, s5, 8
	v_and_or_b32 v2, v2, s36, v31
	v_and_or_b32 v12, v3, s37, v31
	v_lshlrev_b32_e32 v3, 3, v33
	v_or_b32_e32 v34, 8, v33
	s_add_u32 s20, s25, s4
	v_mov_b32_e32 v183, 0
	v_and_or_b32 v20, v3, s36, v31
	v_lshlrev_b32_e32 v3, 3, v34
	s_addc_u32 s21, s26, 0
	v_lshlrev_b32_e32 v180, 12, v2
	v_mov_b32_e32 v181, v183
	v_and_or_b32 v22, v3, s37, v31
	v_lshl_add_u64 v[2:3], s[20:21], 0, v[180:181]
	v_lshlrev_b32_e32 v182, 2, v178
	v_lshl_add_u64 v[10:11], v[2:3], 0, v[182:183]
	v_lshlrev_b32_e32 v184, 12, v12
	v_mov_b32_e32 v185, v183
	s_lshl_b32 s4, s5, 7
	global_load_dwordx4 v[2:5], v[10:11], off offset:16
	global_load_dwordx4 v[6:9], v[10:11], off
	v_lshl_add_u64 v[10:11], s[20:21], 0, v[184:185]
	s_add_u32 s22, s27, s4
	v_lshl_add_u64 v[14:15], v[10:11], 0, v[182:183]
	s_addc_u32 s23, s28, 0
	v_lshlrev_b32_e32 v186, 11, v20
	v_mov_b32_e32 v187, v183
	global_load_dwordx4 v[10:13], v[14:15], off offset:16
	global_load_dwordx4 v[16:19], v[14:15], off
	v_lshl_add_u64 v[20:21], s[22:23], 0, v[186:187]
	v_lshlrev_b32_e32 v14, 1, v178
	v_mov_b32_e32 v15, v183
	v_lshlrev_b32_e32 v188, 11, v22
	v_mov_b32_e32 v189, v183
	v_lshl_add_u64 v[24:25], v[20:21], 0, v[14:15]
	v_lshl_add_u64 v[20:21], s[22:23], 0, v[188:189]
	v_lshl_add_u64 v[26:27], v[20:21], 0, v[14:15]
	global_load_dwordx4 v[20:23], v[24:25], off
	global_load_dwordx4 v[50:53], v[26:27], off
	v_bfe_u32 v24, v0, 5, 1
	v_and_or_b32 v25, v30, 22, v24
	v_lshl_or_b32 v208, v25, 10, v29
	v_and_or_b32 v25, v32, 30, v24
	v_lshl_or_b32 v205, v25, 10, v29
	v_bitop3_b32 v25, s34, 16, v28 bitop3:0x26
	v_and_or_b32 v26, v25, 22, v24
	v_lshl_or_b32 v204, v26, 10, v29
	v_bitop3_b32 v26, s35, v28, 24 bitop3:0xde
	v_and_or_b32 v27, v26, 30, v24
	v_lshl_or_b32 v201, v27, 10, v29
	v_and_or_b32 v27, v33, 22, v24
	v_lshl_or_b32 v206, v27, 10, v29
	v_and_or_b32 v27, v34, 30, v24
	s_load_dwordx8 s[4:11], s[0:1], 0x20
	v_lshl_or_b32 v207, v27, 10, v29
	v_bitop3_b32 v27, s38, 16, v28 bitop3:0x26
	v_bitop3_b32 v28, s39, v28, 24 bitop3:0xde
	v_and_or_b32 v30, v27, 22, v24
	v_and_or_b32 v24, v28, 30, v24
	v_and_b32_e32 v179, 15, v0
	v_lshl_or_b32 v202, v30, 10, v29
	v_lshl_or_b32 v203, v24, 10, v29
	v_lshlrev_b32_e32 v24, 3, v28
	v_lshlrev_b32_e32 v29, 2, v0
	v_lshrrev_b32_e32 v198, 8, v0
	v_lshlrev_b32_e32 v25, 3, v25
	v_lshlrev_b32_e32 v26, 3, v26
	v_lshlrev_b32_e32 v27, 3, v27
	v_and_or_b32 v28, v24, s37, v31
	v_and_b32_e32 v24, 48, v0
	v_and_b32_e32 v29, 32, v29
	v_lshlrev_b32_e32 v30, 6, v179
	s_mov_b32 s29, 0
	v_and_b32_e32 v199, 63, v0
	v_and_or_b32 v25, v25, s36, v31
	v_and_or_b32 v26, v26, s37, v31
	v_bfe_u32 v200, v0, 6, 2
	v_and_or_b32 v27, v27, s36, v31
	v_lshlrev_b32_e32 v80, 14, v198
	v_bitop3_b32 v81, v30, v29, v24 bitop3:0x36
	v_lshlrev_b32_e32 v190, 12, v25
	v_mov_b32_e32 v191, v183
	v_lshl_add_u64 v[24:25], s[20:21], 0, v[190:191]
	v_lshl_add_u64 v[24:25], v[24:25], 0, v[182:183]
	v_lshlrev_b32_e32 v192, 12, v26
	v_mov_b32_e32 v193, v183
	global_load_dwordx4 v[54:57], v[24:25], off offset:16
	global_load_dwordx4 v[58:61], v[24:25], off
	v_lshl_add_u64 v[24:25], s[20:21], 0, v[192:193]
	v_lshl_add_u64 v[24:25], v[24:25], 0, v[182:183]
	v_lshlrev_b32_e32 v194, 11, v27
	v_mov_b32_e32 v195, v183
	global_load_dwordx4 v[62:65], v[24:25], off offset:16
	global_load_dwordx4 v[66:69], v[24:25], off
	v_lshl_add_u64 v[24:25], s[22:23], 0, v[194:195]
	v_lshlrev_b32_e32 v196, 11, v28
	v_mov_b32_e32 v197, v183
	v_lshl_add_u64 v[24:25], v[24:25], 0, v[14:15]
	v_lshl_add_u64 v[26:27], s[22:23], 0, v[196:197]
	v_lshl_add_u64 v[26:27], v[26:27], 0, v[14:15]
	global_load_dwordx4 v[70:73], v[24:25], off
	global_load_dwordx4 v[74:77], v[26:27], off
	s_add_i32 s33, s33, 64
	s_and_b32 s20, s33, 0x3c0
	s_lshl_b32 s0, s20, 2
	s_add_u32 s0, s25, s0
	s_addc_u32 s1, s26, 0
	v_lshl_add_u64 v[24:25], s[0:1], 0, v[180:181]
	v_lshl_add_u64 v[24:25], v[24:25], 0, v[182:183]
	s_lshl_b32 s20, s20, 1
	global_load_dwordx4 v[42:45], v[24:25], off offset:16
	global_load_dwordx4 v[46:49], v[24:25], off
	v_lshl_add_u64 v[24:25], s[0:1], 0, v[184:185]
	s_add_u32 s20, s27, s20
	v_lshl_add_u64 v[24:25], v[24:25], 0, v[182:183]
	s_addc_u32 s21, s28, 0
	global_load_dwordx4 v[34:37], v[24:25], off offset:16
	global_load_dwordx4 v[38:41], v[24:25], off
	v_lshl_add_u64 v[24:25], s[20:21], 0, v[186:187]
	v_lshl_add_u64 v[24:25], v[24:25], 0, v[14:15]
	v_lshl_add_u64 v[26:27], s[20:21], 0, v[188:189]
	v_lshl_add_u64 v[78:79], v[26:27], 0, v[14:15]
	global_load_dwordx4 v[30:33], v[24:25], off
	global_load_dwordx4 v[26:29], v[78:79], off
	s_waitcnt vmcnt(16)
	v_cvt_pk_bf16_f32 v6, v6, v7
	v_cvt_pk_bf16_f32 v7, v8, v9
	v_cvt_pk_bf16_f32 v8, v2, v3
	v_add_u32_e32 v2, 0, v208
	v_cvt_pk_bf16_f32 v9, v4, v5
	ds_write_b128 v2, v[6:9]
	s_waitcnt vmcnt(14)
	v_cvt_pk_bf16_f32 v2, v16, v17
	v_add_u32_e32 v6, 0, v205
	v_cvt_pk_bf16_f32 v3, v18, v19
	v_cvt_pk_bf16_f32 v4, v10, v11
	v_cvt_pk_bf16_f32 v5, v12, v13
	ds_write_b128 v6, v[2:5]
	v_add_u32_e32 v2, 0, v206
	s_waitcnt vmcnt(13)
	ds_write_b128 v2, v[20:23] offset:32768
	v_add_u32_e32 v2, 0, v207
	s_waitcnt vmcnt(12)
	ds_write_b128 v2, v[50:53] offset:32768
	s_waitcnt vmcnt(10)
	v_cvt_pk_bf16_f32 v2, v58, v59
	v_add_u32_e32 v6, 0, v204
	v_cvt_pk_bf16_f32 v3, v60, v61
	v_cvt_pk_bf16_f32 v4, v54, v55
	v_cvt_pk_bf16_f32 v5, v56, v57
	ds_write_b128 v6, v[2:5]
	s_waitcnt vmcnt(8)
	v_cvt_pk_bf16_f32 v2, v66, v67
	v_add_u32_e32 v6, 0, v201
	v_cvt_pk_bf16_f32 v3, v68, v69
	v_cvt_pk_bf16_f32 v4, v62, v63
	v_cvt_pk_bf16_f32 v5, v64, v65
	ds_write_b128 v6, v[2:5]
	v_add_u32_e32 v2, 0, v202
	s_waitcnt vmcnt(7)
	ds_write_b128 v2, v[70:73] offset:32768
	v_add_u32_e32 v2, 0, v203
	s_waitcnt vmcnt(6)
	ds_write_b128 v2, v[74:77] offset:32768
	v_lshl_add_u64 v[2:3], s[0:1], 0, v[190:191]
	v_lshl_add_u64 v[2:3], v[2:3], 0, v[182:183]
	global_load_dwordx4 v[6:9], v[2:3], off offset:16
	global_load_dwordx4 v[22:25], v[2:3], off
	v_lshl_add_u64 v[2:3], s[0:1], 0, v[192:193]
	v_lshl_add_u64 v[16:17], v[2:3], 0, v[182:183]
	global_load_dwordx4 v[2:5], v[16:17], off offset:16
	global_load_dwordx4 v[10:13], v[16:17], off
	v_lshl_add_u64 v[16:17], s[20:21], 0, v[194:195]
	v_lshl_add_u64 v[50:51], v[16:17], 0, v[14:15]
	v_lshl_add_u64 v[16:17], s[20:21], 0, v[196:197]
	v_lshl_add_u64 v[52:53], v[16:17], 0, v[14:15]
	global_load_dwordx4 v[18:21], v[50:51], off
	global_load_dwordx4 v[14:17], v[52:53], off
	v_lshlrev_b32_e32 v50, 13, v200
	s_cmp_lg_u32 0, -1
	s_cselect_b32 s0, 0, 0
	v_add3_u32 v209, v80, s0, v81
	s_add_i32 s0, s0, 0x8000
	v_add3_u32 v210, v50, s0, v81
	s_lshl_b32 s0, s30, 1
	s_add_i32 s31, s31, s0
	s_lshl_b32 s0, s2, 3
	s_add_i32 s0, s0, s31
	s_waitcnt lgkmcnt(0)
	s_and_b32 s0, s0, 15
	s_lshl_b32 s0, s0, 6
	s_add_i32 s22, s0, 0x80
	v_mov_b32_e32 v50, v183
	v_mov_b32_e32 v51, v183
	v_mov_b32_e32 v52, v183
	v_mov_b32_e32 v53, v183
	v_mov_b32_e32 v54, v183
	v_mov_b32_e32 v55, v183
	v_mov_b32_e32 v56, v183
	v_mov_b32_e32 v57, v183
	v_mov_b32_e32 v58, v183
	v_mov_b32_e32 v59, v183
	v_mov_b32_e32 v60, v183
	v_mov_b32_e32 v61, v183
	v_mov_b32_e32 v62, v183
	v_mov_b32_e32 v63, v183
	v_mov_b32_e32 v64, v183
	v_mov_b32_e32 v65, v183
	v_mov_b32_e32 v66, v183
	v_mov_b32_e32 v67, v183
	v_mov_b32_e32 v68, v183
	v_mov_b32_e32 v69, v183
	v_mov_b32_e32 v70, v183
	v_mov_b32_e32 v71, v183
	v_mov_b32_e32 v72, v183
	v_mov_b32_e32 v73, v183
	v_mov_b32_e32 v74, v183
	v_mov_b32_e32 v75, v183
	v_mov_b32_e32 v76, v183
	v_mov_b32_e32 v77, v183
	v_mov_b32_e32 v78, v183
	v_mov_b32_e32 v79, v183
	v_mov_b32_e32 v80, v183
	v_mov_b32_e32 v81, v183
	v_mov_b32_e32 v82, v183
	v_mov_b32_e32 v83, v183
	v_mov_b32_e32 v84, v183
	v_mov_b32_e32 v85, v183
	v_mov_b32_e32 v86, v183
	v_mov_b32_e32 v87, v183
	v_mov_b32_e32 v88, v183
	v_mov_b32_e32 v89, v183
	v_mov_b32_e32 v90, v183
	v_mov_b32_e32 v91, v183
	v_mov_b32_e32 v92, v183
	v_mov_b32_e32 v93, v183
	v_mov_b32_e32 v94, v183
	v_mov_b32_e32 v95, v183
	v_mov_b32_e32 v96, v183
	v_mov_b32_e32 v97, v183
	v_mov_b32_e32 v98, v183
	v_mov_b32_e32 v99, v183
	v_mov_b32_e32 v100, v183
	v_mov_b32_e32 v101, v183
	v_mov_b32_e32 v102, v183
	v_mov_b32_e32 v103, v183
	v_mov_b32_e32 v104, v183
	v_mov_b32_e32 v105, v183
	v_mov_b32_e32 v106, v183
	v_mov_b32_e32 v107, v183
	v_mov_b32_e32 v108, v183
	v_mov_b32_e32 v109, v183
	v_mov_b32_e32 v110, v183
	v_mov_b32_e32 v111, v183
	v_mov_b32_e32 v112, v183
	v_mov_b32_e32 v113, v183
	v_mov_b32_e32 v114, v183
	v_mov_b32_e32 v115, v183
	v_mov_b32_e32 v116, v183
	v_mov_b32_e32 v117, v183
	v_mov_b32_e32 v118, v183
	v_mov_b32_e32 v119, v183
	v_mov_b32_e32 v120, v183
	v_mov_b32_e32 v121, v183
	v_mov_b32_e32 v122, v183
	v_mov_b32_e32 v123, v183
	v_mov_b32_e32 v124, v183
	v_mov_b32_e32 v125, v183
	v_mov_b32_e32 v126, v183
	v_mov_b32_e32 v127, v183
	v_mov_b32_e32 v128, v183
	v_mov_b32_e32 v129, v183
	v_mov_b32_e32 v130, v183
	v_mov_b32_e32 v131, v183
	v_mov_b32_e32 v132, v183
	v_mov_b32_e32 v133, v183
	v_mov_b32_e32 v134, v183
	v_mov_b32_e32 v135, v183
	v_mov_b32_e32 v136, v183
	v_mov_b32_e32 v137, v183
	v_mov_b32_e32 v138, v183
	v_mov_b32_e32 v139, v183
	v_mov_b32_e32 v140, v183
	v_mov_b32_e32 v141, v183
	v_mov_b32_e32 v142, v183
	v_mov_b32_e32 v143, v183
	v_mov_b32_e32 v144, v183
	v_mov_b32_e32 v145, v183
	v_mov_b32_e32 v146, v183
	v_mov_b32_e32 v147, v183
	v_mov_b32_e32 v148, v183
	v_mov_b32_e32 v149, v183
	v_mov_b32_e32 v150, v183
	v_mov_b32_e32 v151, v183
	v_mov_b32_e32 v152, v183
	v_mov_b32_e32 v153, v183
	v_mov_b32_e32 v154, v183
	v_mov_b32_e32 v155, v183
	v_mov_b32_e32 v156, v183
	v_mov_b32_e32 v157, v183
	v_mov_b32_e32 v158, v183
	v_mov_b32_e32 v159, v183
	v_mov_b32_e32 v160, v183
	v_mov_b32_e32 v161, v183
	v_mov_b32_e32 v162, v183
	v_mov_b32_e32 v163, v183
	v_mov_b32_e32 v164, v183
	v_mov_b32_e32 v165, v183
	v_mov_b32_e32 v166, v183
	v_mov_b32_e32 v167, v183
	v_mov_b32_e32 v168, v183
	v_mov_b32_e32 v169, v183
	v_mov_b32_e32 v170, v183
	v_mov_b32_e32 v171, v183
	v_mov_b32_e32 v172, v183
	v_mov_b32_e32 v173, v183
	v_mov_b32_e32 v174, v183
	v_mov_b32_e32 v175, v183
	v_mov_b32_e32 v176, v183
	v_mov_b32_e32 v177, v183
	s_barrier
	s_cmp_lg_u32 s40, 0
	s_cbranch_scc1 .Lrot1_loop

.Lrot1_done:
	s_lshl_b64 s[0:1], s[18:19], 24
	ds_read_b128 v[180:183], v210 offset:0
	ds_read_b128 v[184:187], v210 offset:0x800
	ds_read_b128 v[188:191], v210 offset:0x1000
	ds_read_b128 v[192:195], v210 offset:0x1800
	ds_read_b128 v[212:215], v209 offset:0
	ds_read_b128 v[216:219], v209 offset:0x800
	ds_read_b128 v[220:223], v209 offset:0x1000
	s_waitcnt lgkmcnt(0)
	s_add_u32 s0, s10, s0
	s_addc_u32 s18, s11, s1
	s_lshl_b32 s19, s24, 1
	s_mov_b32 s1, 0
	s_add_u32 s0, s0, s19
	s_waitcnt lgkmcnt(2)
	s_addc_u32 s20, s18, 0
	v_mfma_f32_16x16x32_bf16 v[174:177], v[180:183], v[212:215], v[174:177]
	v_mfma_f32_16x16x32_bf16 v[170:173], v[184:187], v[212:215], v[170:173]
	v_mfma_f32_16x16x32_bf16 v[166:169], v[188:191], v[212:215], v[166:169]
	v_mfma_f32_16x16x32_bf16 v[162:165], v[192:195], v[212:215], v[162:165]
	ds_read_b128 v[212:215], v209 offset:0x1800
	s_waitcnt lgkmcnt(2)
	s_nop 0
	v_mfma_f32_16x16x32_bf16 v[158:161], v[180:183], v[216:219], v[158:161]
	v_mfma_f32_16x16x32_bf16 v[154:157], v[184:187], v[216:219], v[154:157]
	v_mfma_f32_16x16x32_bf16 v[150:153], v[188:191], v[216:219], v[150:153]
	v_mfma_f32_16x16x32_bf16 v[146:149], v[192:195], v[216:219], v[146:149]
	ds_read_b128 v[216:219], v209 offset:0x2000
	s_waitcnt lgkmcnt(2)
	s_nop 0
	v_mfma_f32_16x16x32_bf16 v[142:145], v[180:183], v[220:223], v[142:145]
	v_mfma_f32_16x16x32_bf16 v[138:141], v[184:187], v[220:223], v[138:141]
	v_mfma_f32_16x16x32_bf16 v[134:137], v[188:191], v[220:223], v[134:137]
	v_mfma_f32_16x16x32_bf16 v[130:133], v[192:195], v[220:223], v[130:133]
	ds_read_b128 v[220:223], v209 offset:0x2800
	s_waitcnt lgkmcnt(2)
	s_nop 0
	v_mfma_f32_16x16x32_bf16 v[126:129], v[180:183], v[212:215], v[126:129]
	v_mfma_f32_16x16x32_bf16 v[122:125], v[184:187], v[212:215], v[122:125]
	v_mfma_f32_16x16x32_bf16 v[118:121], v[188:191], v[212:215], v[118:121]
	v_mfma_f32_16x16x32_bf16 v[114:117], v[192:195], v[212:215], v[114:117]
	ds_read_b128 v[212:215], v209 offset:0x3000
	s_waitcnt lgkmcnt(2)
	s_nop 0
	v_mfma_f32_16x16x32_bf16 v[110:113], v[180:183], v[216:219], v[110:113]
	v_mfma_f32_16x16x32_bf16 v[106:109], v[184:187], v[216:219], v[106:109]
	v_mfma_f32_16x16x32_bf16 v[102:105], v[188:191], v[216:219], v[102:105]
	v_mfma_f32_16x16x32_bf16 v[98:101], v[192:195], v[216:219], v[98:101]
	ds_read_b128 v[216:219], v209 offset:0x3800
	s_waitcnt lgkmcnt(2)
	s_nop 0
	v_mfma_f32_16x16x32_bf16 v[94:97], v[180:183], v[220:223], v[94:97]
	v_mfma_f32_16x16x32_bf16 v[90:93], v[184:187], v[220:223], v[90:93]
	v_mfma_f32_16x16x32_bf16 v[86:89], v[188:191], v[220:223], v[86:89]
	v_mfma_f32_16x16x32_bf16 v[82:85], v[192:195], v[220:223], v[82:85]
	s_waitcnt lgkmcnt(1)
	s_nop 0
	v_mfma_f32_16x16x32_bf16 v[78:81], v[180:183], v[212:215], v[78:81]
	v_mfma_f32_16x16x32_bf16 v[74:77], v[184:187], v[212:215], v[74:77]
	v_mfma_f32_16x16x32_bf16 v[70:73], v[188:191], v[212:215], v[70:73]
	v_mfma_f32_16x16x32_bf16 v[66:69], v[192:195], v[212:215], v[66:69]
	s_waitcnt lgkmcnt(0)
	s_nop 0
	v_mfma_f32_16x16x32_bf16 v[62:65], v[180:183], v[216:219], v[62:65]
	v_mfma_f32_16x16x32_bf16 v[58:61], v[184:187], v[216:219], v[58:61]
	v_mfma_f32_16x16x32_bf16 v[54:57], v[188:191], v[216:219], v[54:57]
	v_mfma_f32_16x16x32_bf16 v[50:53], v[192:195], v[216:219], v[50:53]
	s_add_i32 s18, 0, 0x10000
	s_waitcnt vmcnt(10)
	v_cvt_pk_bf16_f32 v46, v46, v47
	v_cvt_pk_bf16_f32 v47, v48, v49
	v_cvt_pk_bf16_f32 v48, v42, v43
	v_add_u32_e32 v42, s18, v208
	s_waitcnt vmcnt(8)
	v_cvt_pk_bf16_f32 v38, v38, v39
	v_cvt_pk_bf16_f32 v39, v40, v41
	v_cvt_pk_bf16_f32 v40, v34, v35
	v_add_u32_e32 v34, s18, v205
	s_add_i32 s19, 0, 0x18000
	v_cvt_pk_bf16_f32 v49, v44, v45
	ds_write_b128 v42, v[46:49]
	v_cvt_pk_bf16_f32 v41, v36, v37
	ds_write_b128 v34, v[38:41]
	v_add_u32_e32 v34, s19, v206
	s_waitcnt vmcnt(7)
	ds_write_b128 v34, v[30:33]
	v_add_u32_e32 v30, s19, v207
	s_waitcnt vmcnt(6)
	ds_write_b128 v30, v[26:29]
	ds_read_b128 v[26:29], v210 offset:0x400
	ds_read_b128 v[30:33], v210 offset:0xc00
	ds_read_b128 v[34:37], v210 offset:0x1400
	ds_read_b128 v[38:41], v210 offset:0x1c00
	ds_read_b128 v[42:45], v209 offset:0x400
	ds_read_b128 v[46:49], v209 offset:0xc00
	ds_read_b128 v[180:183], v209 offset:0x1400
	s_nop 0
	s_waitcnt lgkmcnt(2)
	s_nop 0
	v_mfma_f32_16x16x32_bf16 v[174:177], v[26:29], v[42:45], v[174:177]
	v_mfma_f32_16x16x32_bf16 v[170:173], v[30:33], v[42:45], v[170:173]
	v_mfma_f32_16x16x32_bf16 v[166:169], v[34:37], v[42:45], v[166:169]
	v_mfma_f32_16x16x32_bf16 v[42:45], v[38:41], v[42:45], v[162:165]
	ds_read_b128 v[162:165], v209 offset:0x1c00
	s_waitcnt lgkmcnt(2)
	s_nop 0
	v_mfma_f32_16x16x32_bf16 v[158:161], v[26:29], v[46:49], v[158:161]
	v_mfma_f32_16x16x32_bf16 v[154:157], v[30:33], v[46:49], v[154:157]
	v_mfma_f32_16x16x32_bf16 v[150:153], v[34:37], v[46:49], v[150:153]
	v_mfma_f32_16x16x32_bf16 v[46:49], v[38:41], v[46:49], v[146:149]
	ds_read_b128 v[146:149], v209 offset:0x2400
	s_waitcnt lgkmcnt(2)
	s_nop 0
	v_mfma_f32_16x16x32_bf16 v[142:145], v[26:29], v[180:183], v[142:145]
	v_mfma_f32_16x16x32_bf16 v[138:141], v[30:33], v[180:183], v[138:141]
	v_mfma_f32_16x16x32_bf16 v[134:137], v[34:37], v[180:183], v[134:137]
	v_mfma_f32_16x16x32_bf16 v[130:133], v[38:41], v[180:183], v[130:133]
	ds_read_b128 v[180:183], v209 offset:0x2c00
	s_waitcnt lgkmcnt(2)
	s_nop 0
	v_mfma_f32_16x16x32_bf16 v[126:129], v[26:29], v[162:165], v[126:129]
	v_mfma_f32_16x16x32_bf16 v[122:125], v[30:33], v[162:165], v[122:125]
	v_mfma_f32_16x16x32_bf16 v[118:121], v[34:37], v[162:165], v[118:121]
	v_mfma_f32_16x16x32_bf16 v[114:117], v[38:41], v[162:165], v[114:117]
	ds_read_b128 v[162:165], v209 offset:0x3400
	s_waitcnt lgkmcnt(2)
	s_nop 0
	v_mfma_f32_16x16x32_bf16 v[110:113], v[26:29], v[146:149], v[110:113]
	v_mfma_f32_16x16x32_bf16 v[106:109], v[30:33], v[146:149], v[106:109]
	v_mfma_f32_16x16x32_bf16 v[102:105], v[34:37], v[146:149], v[102:105]
	v_mfma_f32_16x16x32_bf16 v[98:101], v[38:41], v[146:149], v[98:101]
	ds_read_b128 v[146:149], v209 offset:0x3c00
	s_waitcnt lgkmcnt(2)
	s_nop 0
	v_mfma_f32_16x16x32_bf16 v[94:97], v[26:29], v[180:183], v[94:97]
	v_mfma_f32_16x16x32_bf16 v[90:93], v[30:33], v[180:183], v[90:93]
	v_mfma_f32_16x16x32_bf16 v[86:89], v[34:37], v[180:183], v[86:89]
	v_mfma_f32_16x16x32_bf16 v[82:85], v[38:41], v[180:183], v[82:85]
	s_waitcnt lgkmcnt(1)
	s_nop 0
	v_mfma_f32_16x16x32_bf16 v[78:81], v[26:29], v[162:165], v[78:81]
	v_mfma_f32_16x16x32_bf16 v[74:77], v[30:33], v[162:165], v[74:77]
	v_mfma_f32_16x16x32_bf16 v[70:73], v[34:37], v[162:165], v[70:73]
	v_mfma_f32_16x16x32_bf16 v[66:69], v[38:41], v[162:165], v[66:69]
	s_waitcnt lgkmcnt(0)
	s_nop 0
	v_mfma_f32_16x16x32_bf16 v[26:29], v[26:29], v[146:149], v[62:65]
	v_mfma_f32_16x16x32_bf16 v[30:33], v[30:33], v[146:149], v[58:61]
	v_mfma_f32_16x16x32_bf16 v[34:37], v[34:37], v[146:149], v[54:57]
	v_mfma_f32_16x16x32_bf16 v[38:41], v[38:41], v[146:149], v[50:53]
	s_waitcnt vmcnt(4)
	v_cvt_pk_bf16_f32 v22, v22, v23
	v_cvt_pk_bf16_f32 v23, v24, v25
	v_cvt_pk_bf16_f32 v24, v6, v7
	v_cvt_pk_bf16_f32 v25, v8, v9
	v_add_u32_e32 v6, s18, v204
	s_waitcnt vmcnt(3)
	v_cvt_pk_bf16_f32 v8, v2, v3
	v_add_u32_e32 v2, s18, v201
	ds_write_b128 v6, v[22:25]
	s_waitcnt vmcnt(2)
	v_cvt_pk_bf16_f32 v6, v10, v11
	v_cvt_pk_bf16_f32 v7, v12, v13
	v_cvt_pk_bf16_f32 v9, v4, v5
	ds_write_b128 v2, v[6:9]
	v_add_u32_e32 v2, s19, v202
	s_waitcnt vmcnt(1)
	ds_write_b128 v2, v[18:21]
	v_add_u32_e32 v2, s19, v203
	s_waitcnt vmcnt(0)
	ds_write_b128 v2, v[14:17]
	s_waitcnt lgkmcnt(0)
	s_barrier
	v_add_u32_e32 v178, 0x10000, v209
	v_add_u32_e32 v196, 0x10000, v210
	ds_read_b128 v[2:5], v196 offset:0
	ds_read_b128 v[6:9], v196 offset:0x800
	ds_read_b128 v[10:13], v196 offset:0x1000
	ds_read_b128 v[14:17], v196 offset:0x1800
	ds_read_b128 v[18:21], v178 offset:0
	s_and_b64 s[16:17], s[16:17], exec
	ds_read_b128 v[22:25], v178 offset:0x800
	ds_read_b128 v[50:53], v178 offset:0x1000
	s_waitcnt lgkmcnt(2)
	s_cselect_b32 s5, s5, s7
	s_cselect_b32 s4, s4, s6
	s_lshl_b32 s6, s3, 10
	v_mfma_f32_16x16x32_bf16 v[54:57], v[2:5], v[18:21], v[174:177]
	s_add_u32 s6, s4, s6
	s_addc_u32 s7, s5, 0
	s_lshl_b32 s3, s3, 9
	v_mfma_f32_16x16x32_bf16 v[58:61], v[6:9], v[18:21], v[170:173]
	s_add_u32 s4, s0, s3
	s_addc_u32 s5, s20, 0
	v_mfma_f32_16x16x32_bf16 v[62:65], v[10:13], v[18:21], v[166:169]
	v_mfma_f32_16x16x32_bf16 v[18:21], v[14:17], v[18:21], v[42:45]
	ds_read_b128 v[42:45], v178 offset:0x1800
	s_waitcnt lgkmcnt(2)
	s_nop 0
	v_mfma_f32_16x16x32_bf16 v[146:149], v[2:5], v[22:25], v[158:161]
	v_mfma_f32_16x16x32_bf16 v[154:157], v[6:9], v[22:25], v[154:157]
	v_mfma_f32_16x16x32_bf16 v[150:153], v[10:13], v[22:25], v[150:153]
	v_mfma_f32_16x16x32_bf16 v[22:25], v[14:17], v[22:25], v[46:49]
	ds_read_b128 v[46:49], v178 offset:0x2000
	s_waitcnt lgkmcnt(2)
	s_nop 0
	v_mfma_f32_16x16x32_bf16 v[142:145], v[2:5], v[50:53], v[142:145]
	v_mfma_f32_16x16x32_bf16 v[138:141], v[6:9], v[50:53], v[138:141]
	v_mfma_f32_16x16x32_bf16 v[134:137], v[10:13], v[50:53], v[134:137]
	v_mfma_f32_16x16x32_bf16 v[50:53], v[14:17], v[50:53], v[130:133]
	ds_read_b128 v[130:133], v178 offset:0x2800
	s_waitcnt lgkmcnt(2)
	s_nop 0
	v_mfma_f32_16x16x32_bf16 v[126:129], v[2:5], v[42:45], v[126:129]
	v_mfma_f32_16x16x32_bf16 v[122:125], v[6:9], v[42:45], v[122:125]
	v_mfma_f32_16x16x32_bf16 v[118:121], v[10:13], v[42:45], v[118:121]
	v_mfma_f32_16x16x32_bf16 v[42:45], v[14:17], v[42:45], v[114:117]
	ds_read_b128 v[114:117], v178 offset:0x3000
	s_waitcnt lgkmcnt(2)
	s_nop 0
	v_mfma_f32_16x16x32_bf16 v[110:113], v[2:5], v[46:49], v[110:113]
	v_mfma_f32_16x16x32_bf16 v[106:109], v[6:9], v[46:49], v[106:109]
	v_mfma_f32_16x16x32_bf16 v[102:105], v[10:13], v[46:49], v[102:105]
	v_mfma_f32_16x16x32_bf16 v[98:101], v[14:17], v[46:49], v[98:101]
	ds_read_b128 v[46:49], v178 offset:0x3800
	s_waitcnt lgkmcnt(2)
	s_nop 0
	v_mfma_f32_16x16x32_bf16 v[158:161], v[2:5], v[130:133], v[94:97]
	v_mfma_f32_16x16x32_bf16 v[162:165], v[6:9], v[130:133], v[90:93]
	v_mfma_f32_16x16x32_bf16 v[166:169], v[10:13], v[130:133], v[86:89]
	v_mfma_f32_16x16x32_bf16 v[130:133], v[14:17], v[130:133], v[82:85]
	s_waitcnt lgkmcnt(1)
	s_nop 0
	v_mfma_f32_16x16x32_bf16 v[66:69], v[14:17], v[114:117], v[66:69]
	v_mfma_f32_16x16x32_bf16 v[170:173], v[2:5], v[114:117], v[78:81]
	v_mfma_f32_16x16x32_bf16 v[174:177], v[6:9], v[114:117], v[74:77]
	v_mfma_f32_16x16x32_bf16 v[180:183], v[10:13], v[114:117], v[70:73]
	s_waitcnt lgkmcnt(0)
	s_nop 0
	v_mfma_f32_16x16x32_bf16 v[2:5], v[2:5], v[46:49], v[26:29]
	v_mfma_f32_16x16x32_bf16 v[114:117], v[6:9], v[46:49], v[30:33]
	v_mfma_f32_16x16x32_bf16 v[34:37], v[10:13], v[46:49], v[34:37]
	v_mfma_f32_16x16x32_bf16 v[184:187], v[14:17], v[46:49], v[38:41]
	ds_read_b128 v[188:191], v196 offset:0x400
	ds_read_b128 v[192:195], v196 offset:0xc00
	ds_read_b128 v[202:205], v196 offset:0x1400
	ds_read_b128 v[206:209], v196 offset:0x1c00
	ds_read_b128 v[6:9], v178 offset:0x400
	ds_read_b128 v[10:13], v178 offset:0xc00
	ds_read_b128 v[14:17], v178 offset:0x1400
	s_nop 0
	s_waitcnt lgkmcnt(2)
	s_nop 0
	v_mfma_f32_16x16x32_bf16 v[94:97], v[192:195], v[6:9], v[58:61]
	v_mfma_f32_16x16x32_bf16 v[62:65], v[202:205], v[6:9], v[62:65]
	v_mfma_f32_16x16x32_bf16 v[30:33], v[206:209], v[6:9], v[18:21]
	v_mfma_f32_16x16x32_bf16 v[210:213], v[188:191], v[6:9], v[54:57]
	ds_read_b128 v[6:9], v178 offset:0x1c00
	s_waitcnt lgkmcnt(2)
	s_nop 0
	v_mfma_f32_16x16x32_bf16 v[90:93], v[192:195], v[10:13], v[154:157]
	v_mfma_f32_16x16x32_bf16 v[58:61], v[202:205], v[10:13], v[150:153]
	v_mfma_f32_16x16x32_bf16 v[26:29], v[206:209], v[10:13], v[22:25]
	v_mfma_f32_16x16x32_bf16 v[146:149], v[188:191], v[10:13], v[146:149]
	ds_read_b128 v[10:13], v178 offset:0x2400
	s_waitcnt lgkmcnt(2)
	s_nop 0
	v_mfma_f32_16x16x32_bf16 v[86:89], v[192:195], v[14:17], v[138:141]
	v_mfma_f32_16x16x32_bf16 v[54:57], v[202:205], v[14:17], v[134:137]
	v_mfma_f32_16x16x32_bf16 v[22:25], v[206:209], v[14:17], v[50:53]
	v_mfma_f32_16x16x32_bf16 v[142:145], v[188:191], v[14:17], v[142:145]
	ds_read_b128 v[38:41], v178 offset:0x2c00
	s_waitcnt lgkmcnt(2)
	s_nop 0
	v_mfma_f32_16x16x32_bf16 v[126:129], v[188:191], v[6:9], v[126:129]
	v_mfma_f32_16x16x32_bf16 v[82:85], v[192:195], v[6:9], v[122:125]
	v_mfma_f32_16x16x32_bf16 v[50:53], v[202:205], v[6:9], v[118:121]
	v_mfma_f32_16x16x32_bf16 v[18:21], v[206:209], v[6:9], v[42:45]
	ds_read_b128 v[6:9], v178 offset:0x3400
	s_waitcnt lgkmcnt(2)
	s_nop 0
	v_mfma_f32_16x16x32_bf16 v[110:113], v[188:191], v[10:13], v[110:113]
	v_mfma_f32_16x16x32_bf16 v[78:81], v[192:195], v[10:13], v[106:109]
	v_mfma_f32_16x16x32_bf16 v[46:49], v[202:205], v[10:13], v[102:105]
	v_mfma_f32_16x16x32_bf16 v[14:17], v[206:209], v[10:13], v[98:101]
	ds_read_b128 v[98:101], v178 offset:0x3c00
	s_waitcnt lgkmcnt(2)
	s_nop 0
	v_mfma_f32_16x16x32_bf16 v[106:109], v[188:191], v[38:41], v[158:161]
	v_mfma_f32_16x16x32_bf16 v[74:77], v[192:195], v[38:41], v[162:165]
	v_mfma_f32_16x16x32_bf16 v[42:45], v[202:205], v[38:41], v[166:169]
	v_mfma_f32_16x16x32_bf16 v[10:13], v[206:209], v[38:41], v[130:133]
	s_waitcnt lgkmcnt(1)
	s_nop 0
	v_mfma_f32_16x16x32_bf16 v[118:121], v[188:191], v[6:9], v[170:173]
	v_mfma_f32_16x16x32_bf16 v[70:73], v[192:195], v[6:9], v[174:177]
	v_mfma_f32_16x16x32_bf16 v[38:41], v[202:205], v[6:9], v[180:183]
	v_mfma_f32_16x16x32_bf16 v[6:9], v[206:209], v[6:9], v[66:69]
	s_waitcnt lgkmcnt(0)
	s_nop 0
	v_mfma_f32_16x16x32_bf16 v[122:125], v[188:191], v[98:101], v[2:5]
	v_mfma_f32_16x16x32_bf16 v[66:69], v[192:195], v[98:101], v[114:117]
	v_mfma_f32_16x16x32_bf16 v[34:37], v[202:205], v[98:101], v[34:37]
	v_mfma_f32_16x16x32_bf16 v[2:5], v[206:209], v[98:101], v[184:187]
	v_lshrrev_b32_e32 v98, 2, v199
	v_and_b32_e32 v98, 12, v98
	v_lshl_or_b32 v104, v200, 6, v98
	v_lshlrev_b32_e32 v105, 2, v104
	s_waitcnt lgkmcnt(0)
	s_barrier
	global_load_dwordx4 v[114:117], v105, s[6:7]
	v_lshrrev_b32_e32 v98, 1, v199
	v_lshlrev_b32_e32 v99, 16, v198
	v_lshlrev_b32_e32 v100, 9, v179
	v_and_b32_e32 v102, 8, v98
	v_lshrrev_b32_e32 v98, 3, v104
	v_add3_u32 v103, 0, v99, v100
	v_xor_b32_e32 v130, v98, v179
	v_bitop3_b32 v131, v98, v179, 16 bitop3:0x1e
	global_load_dwordx4 v[98:101], v105, s[6:7] offset:64
	v_lshlrev_b32_e32 v130, 4, v130
	v_lshlrev_b32_e32 v131, 4, v131
	v_add3_u32 v130, v103, v130, v102
	v_add3_u32 v131, v103, v131, v102
	s_movk_i32 s0, 0x200
	s_waitcnt vmcnt(1)
	v_add_f32_e32 v132, v210, v114
	v_add_f32_e32 v133, v211, v115
	v_add_f32_e32 v134, v212, v116
	v_add_f32_e32 v135, v213, v117
	v_add_f32_e32 v140, v142, v114
	v_add_f32_e32 v141, v143, v115
	v_add_f32_e32 v142, v144, v116
	v_add_f32_e32 v143, v145, v117
	v_add_f32_e32 v110, v110, v114
	v_add_f32_e32 v111, v111, v115
	v_add_f32_e32 v106, v106, v114
	v_add_f32_e32 v107, v107, v115
	v_add_f32_e32 v136, v146, v114
	v_add_f32_e32 v137, v147, v115
	v_add_f32_e32 v138, v148, v116
	v_add_f32_e32 v139, v149, v117
	v_add_f32_e32 v126, v126, v114
	v_add_f32_e32 v127, v127, v115
	v_add_f32_e32 v128, v128, v116
	v_add_f32_e32 v129, v129, v117
	v_add_f32_e32 v112, v112, v116
	v_add_f32_e32 v113, v113, v117
	v_add_f32_e32 v108, v108, v116
	v_add_f32_e32 v109, v109, v117
	v_max_f32_e32 v132, 0, v132
	v_max_f32_e32 v133, 0, v133
	v_max_f32_e32 v134, 0, v134
	v_max_f32_e32 v135, 0, v135
	v_max_f32_e32 v140, 0, v140
	v_max_f32_e32 v141, 0, v141
	v_max_f32_e32 v142, 0, v142
	v_max_f32_e32 v143, 0, v143
	v_max_f32_e32 v144, 0, v110
	v_max_f32_e32 v145, 0, v111
	v_max_f32_e32 v148, 0, v106
	v_max_f32_e32 v149, 0, v107
	v_cvt_pk_bf16_f32 v106, v132, v133
	v_cvt_pk_bf16_f32 v107, v134, v135
	v_cvt_pk_bf16_f32 v110, v140, v141
	v_cvt_pk_bf16_f32 v111, v142, v143
	v_add_f32_e32 v118, v118, v114
	v_add_f32_e32 v119, v119, v115
	v_max_f32_e32 v136, 0, v136
	v_max_f32_e32 v137, 0, v137
	v_max_f32_e32 v138, 0, v138
	v_max_f32_e32 v139, 0, v139
	v_max_f32_e32 v126, 0, v126
	v_max_f32_e32 v127, 0, v127
	v_max_f32_e32 v128, 0, v128
	v_max_f32_e32 v129, 0, v129
	v_max_f32_e32 v146, 0, v112
	v_max_f32_e32 v147, 0, v113
	v_max_f32_e32 v150, 0, v108
	v_max_f32_e32 v151, 0, v109
	v_cvt_pk_bf16_f32 v108, v136, v137
	v_cvt_pk_bf16_f32 v109, v138, v139
	v_cvt_pk_bf16_f32 v112, v126, v127
	v_cvt_pk_bf16_f32 v113, v128, v129
	ds_write2st64_b64 v130, v[106:107], v[110:111] offset1:32
	ds_write2st64_b64 v131, v[108:109], v[112:113] offset0:16 offset1:48
	v_add_f32_e32 v106, v121, v117
	v_add_f32_e32 v120, v120, v116
	v_max_f32_e32 v152, 0, v118
	v_max_f32_e32 v153, 0, v119
	v_max_f32_e32 v107, 0, v106
	v_cvt_pk_bf16_f32 v106, v152, v153
	v_max_f32_e32 v120, 0, v120
	v_cvt_pk_bf16_f32 v118, v144, v145
	v_cvt_pk_bf16_f32 v119, v146, v147
	v_cvt_pk_bf16_f32 v107, v120, v107
	ds_write2st64_b64 v130, v[118:119], v[106:107] offset0:64 offset1:96
	v_add_f32_e32 v106, v122, v114
	v_max_f32_e32 v106, 0, v106
	v_add_f32_e32 v107, v123, v115
	v_max_f32_e32 v107, 0, v107
	v_add_f32_e32 v108, v124, v116
	v_add_f32_e32 v109, v125, v117
	v_cvt_pk_bf16_f32 v106, v106, v107
	v_cvt_pk_bf16_f32 v126, v148, v149
	v_cvt_pk_bf16_f32 v127, v150, v151
	v_max_f32_e32 v108, 0, v108
	v_max_f32_e32 v109, 0, v109
	v_cvt_pk_bf16_f32 v107, v108, v109
	ds_write2st64_b64 v131, v[126:127], v[106:107] offset0:80 offset1:112
	v_or_b32_e32 v106, 16, v104
	s_waitcnt vmcnt(0)
	v_add_f32_e32 v94, v94, v98
	v_add_f32_e32 v95, v95, v99
	v_add_f32_e32 v96, v96, v100
	v_lshrrev_b32_e32 v106, 3, v106
	v_max_f32_e32 v94, 0, v94
	v_max_f32_e32 v95, 0, v95
	v_max_f32_e32 v96, 0, v96
	v_add_f32_e32 v97, v97, v101
	v_max_f32_e32 v97, 0, v97
	v_cvt_pk_bf16_f32 v94, v94, v95
	v_cvt_pk_bf16_f32 v95, v96, v97
	v_xor_b32_e32 v96, v106, v179
	v_lshlrev_b32_e32 v96, 4, v96
	v_add3_u32 v107, v103, v96, v102
	v_add_f32_e32 v90, v90, v98
	v_add_f32_e32 v91, v91, v99
	v_add_f32_e32 v92, v92, v100
	ds_write_b64 v107, v[94:95]
	v_max_f32_e32 v90, 0, v90
	v_max_f32_e32 v91, 0, v91
	global_load_dwordx4 v[94:97], v105, s[6:7] offset:128
	v_max_f32_e32 v92, 0, v92
	v_add_f32_e32 v93, v93, v101
	v_max_f32_e32 v93, 0, v93
	v_cvt_pk_bf16_f32 v90, v90, v91
	v_cvt_pk_bf16_f32 v91, v92, v93
	v_bitop3_b32 v92, v106, v179, 16 bitop3:0x1e
	v_add_f32_e32 v66, v66, v98
	v_lshlrev_b32_e32 v92, 4, v92
	v_add_f32_e32 v86, v86, v98
	v_add_f32_e32 v87, v87, v99
	v_add_f32_e32 v82, v82, v98
	v_add_f32_e32 v83, v83, v99
	v_add_f32_e32 v78, v78, v98
	v_add_f32_e32 v79, v79, v99
	v_add_f32_e32 v74, v74, v98
	v_add_f32_e32 v75, v75, v99
	v_add_f32_e32 v70, v70, v98
	v_add_f32_e32 v71, v71, v99
	v_max_f32_e32 v66, 0, v66
	v_add_f32_e32 v67, v67, v99
	v_add3_u32 v92, v103, v92, v102
	v_max_f32_e32 v86, 0, v86
	v_max_f32_e32 v87, 0, v87
	v_add_f32_e32 v88, v88, v100
	v_add_f32_e32 v89, v89, v101
	v_max_f32_e32 v82, 0, v82
	v_max_f32_e32 v83, 0, v83
	v_add_f32_e32 v84, v84, v100
	v_add_f32_e32 v85, v85, v101
	v_max_f32_e32 v78, 0, v78
	v_max_f32_e32 v79, 0, v79
	v_add_f32_e32 v80, v80, v100
	v_add_f32_e32 v81, v81, v101
	v_max_f32_e32 v74, 0, v74
	v_max_f32_e32 v75, 0, v75
	v_add_f32_e32 v76, v76, v100
	v_add_f32_e32 v77, v77, v101
	v_max_f32_e32 v70, 0, v70
	v_max_f32_e32 v71, 0, v71
	v_add_f32_e32 v72, v72, v100
	v_add_f32_e32 v73, v73, v101
	v_max_f32_e32 v67, 0, v67
	v_add_f32_e32 v68, v68, v100
	v_add_f32_e32 v69, v69, v101
	v_cvt_pk_bf16_f32 v66, v66, v67
	ds_write_b64 v92, v[90:91] offset:8192
	v_max_f32_e32 v88, 0, v88
	v_max_f32_e32 v89, 0, v89
	v_cvt_pk_bf16_f32 v86, v86, v87
	v_cvt_pk_bf16_f32 v87, v88, v89
	ds_write_b64 v107, v[86:87] offset:16384
	v_max_f32_e32 v84, 0, v84
	v_max_f32_e32 v85, 0, v85
	v_cvt_pk_bf16_f32 v82, v82, v83
	v_cvt_pk_bf16_f32 v83, v84, v85
	ds_write_b64 v92, v[82:83] offset:24576
	v_max_f32_e32 v80, 0, v80
	v_max_f32_e32 v81, 0, v81
	v_cvt_pk_bf16_f32 v78, v78, v79
	v_cvt_pk_bf16_f32 v79, v80, v81
	ds_write_b64 v107, v[78:79] offset:32768
	v_max_f32_e32 v76, 0, v76
	v_max_f32_e32 v77, 0, v77
	v_cvt_pk_bf16_f32 v74, v74, v75
	v_cvt_pk_bf16_f32 v75, v76, v77
	ds_write_b64 v92, v[74:75] offset:40960
	v_max_f32_e32 v72, 0, v72
	v_max_f32_e32 v73, 0, v73
	v_cvt_pk_bf16_f32 v70, v70, v71
	v_cvt_pk_bf16_f32 v71, v72, v73
	ds_write_b64 v107, v[70:71] offset:49152
	v_max_f32_e32 v68, 0, v68
	v_max_f32_e32 v69, 0, v69
	v_cvt_pk_bf16_f32 v67, v68, v69
	ds_write_b64 v92, v[66:67] offset:57344
	v_or_b32_e32 v66, 32, v104
	v_lshrrev_b32_e32 v70, 3, v66
	global_load_dwordx4 v[66:69], v105, s[6:7] offset:192
	s_waitcnt vmcnt(1)
	v_add_f32_e32 v62, v62, v94
	v_add_f32_e32 v63, v63, v95
	v_add_f32_e32 v64, v64, v96
	v_add_f32_e32 v58, v58, v94
	v_add_f32_e32 v59, v59, v95
	v_add_f32_e32 v60, v60, v96
	v_max_f32_e32 v62, 0, v62
	v_max_f32_e32 v63, 0, v63
	v_max_f32_e32 v64, 0, v64
	v_add_f32_e32 v65, v65, v97
	v_max_f32_e32 v58, 0, v58
	v_max_f32_e32 v59, 0, v59
	v_max_f32_e32 v60, 0, v60
	v_add_f32_e32 v61, v61, v97
	v_max_f32_e32 v65, 0, v65
	v_cvt_pk_bf16_f32 v62, v62, v63
	v_cvt_pk_bf16_f32 v63, v64, v65
	v_xor_b32_e32 v64, v70, v179
	v_max_f32_e32 v61, 0, v61
	v_cvt_pk_bf16_f32 v58, v58, v59
	v_cvt_pk_bf16_f32 v59, v60, v61
	v_bitop3_b32 v60, v70, v179, 16 bitop3:0x1e
	v_add_f32_e32 v34, v34, v94
	v_lshlrev_b32_e32 v64, 4, v64
	v_lshlrev_b32_e32 v60, 4, v60
	v_add_f32_e32 v54, v54, v94
	v_add_f32_e32 v55, v55, v95
	v_add_f32_e32 v50, v50, v94
	v_add_f32_e32 v51, v51, v95
	v_add_f32_e32 v46, v46, v94
	v_add_f32_e32 v47, v47, v95
	v_add_f32_e32 v42, v42, v94
	v_add_f32_e32 v43, v43, v95
	v_add_f32_e32 v38, v38, v94
	v_add_f32_e32 v39, v39, v95
	v_max_f32_e32 v34, 0, v34
	v_add_f32_e32 v35, v35, v95
	v_add3_u32 v64, v103, v64, v102
	v_add3_u32 v60, v103, v60, v102
	v_max_f32_e32 v54, 0, v54
	v_max_f32_e32 v55, 0, v55
	v_add_f32_e32 v56, v56, v96
	v_add_f32_e32 v57, v57, v97
	v_max_f32_e32 v50, 0, v50
	v_max_f32_e32 v51, 0, v51
	v_add_f32_e32 v52, v52, v96
	v_add_f32_e32 v53, v53, v97
	v_max_f32_e32 v46, 0, v46
	v_max_f32_e32 v47, 0, v47
	v_add_f32_e32 v48, v48, v96
	v_add_f32_e32 v49, v49, v97
	v_max_f32_e32 v42, 0, v42
	v_max_f32_e32 v43, 0, v43
	v_add_f32_e32 v44, v44, v96
	v_add_f32_e32 v45, v45, v97
	v_max_f32_e32 v38, 0, v38
	v_max_f32_e32 v39, 0, v39
	v_add_f32_e32 v40, v40, v96
	v_add_f32_e32 v41, v41, v97
	v_max_f32_e32 v35, 0, v35
	v_add_f32_e32 v36, v36, v96
	v_add_f32_e32 v37, v37, v97
	v_cvt_pk_bf16_f32 v34, v34, v35
	ds_write_b64 v64, v[62:63]
	ds_write_b64 v60, v[58:59] offset:8192
	v_max_f32_e32 v56, 0, v56
	v_max_f32_e32 v57, 0, v57
	v_cvt_pk_bf16_f32 v54, v54, v55
	v_cvt_pk_bf16_f32 v55, v56, v57
	ds_write_b64 v64, v[54:55] offset:16384
	v_max_f32_e32 v52, 0, v52
	v_max_f32_e32 v53, 0, v53
	v_cvt_pk_bf16_f32 v50, v50, v51
	v_cvt_pk_bf16_f32 v51, v52, v53
	ds_write_b64 v60, v[50:51] offset:24576
	v_max_f32_e32 v48, 0, v48
	v_max_f32_e32 v49, 0, v49
	v_cvt_pk_bf16_f32 v46, v46, v47
	v_cvt_pk_bf16_f32 v47, v48, v49
	ds_write_b64 v64, v[46:47] offset:32768
	v_max_f32_e32 v44, 0, v44
	v_max_f32_e32 v45, 0, v45
	v_cvt_pk_bf16_f32 v42, v42, v43
	v_cvt_pk_bf16_f32 v43, v44, v45
	ds_write_b64 v60, v[42:43] offset:40960
	v_max_f32_e32 v40, 0, v40
	v_max_f32_e32 v41, 0, v41
	v_cvt_pk_bf16_f32 v38, v38, v39
	v_cvt_pk_bf16_f32 v39, v40, v41
	ds_write_b64 v64, v[38:39] offset:49152
	v_max_f32_e32 v36, 0, v36
	v_max_f32_e32 v37, 0, v37
	v_cvt_pk_bf16_f32 v35, v36, v37
	ds_write_b64 v60, v[34:35] offset:57344
	v_or_b32_e32 v34, 48, v104
	s_waitcnt vmcnt(0)
	v_add_f32_e32 v30, v30, v66
	v_add_f32_e32 v31, v31, v67
	v_add_f32_e32 v32, v32, v68
	v_add_f32_e32 v26, v26, v66
	v_add_f32_e32 v27, v27, v67
	v_add_f32_e32 v28, v28, v68
	v_lshrrev_b32_e32 v34, 3, v34
	v_max_f32_e32 v30, 0, v30
	v_max_f32_e32 v31, 0, v31
	v_max_f32_e32 v32, 0, v32
	v_add_f32_e32 v33, v33, v69
	v_max_f32_e32 v26, 0, v26
	v_max_f32_e32 v27, 0, v27
	v_max_f32_e32 v28, 0, v28
	v_add_f32_e32 v29, v29, v69
	v_max_f32_e32 v33, 0, v33
	v_cvt_pk_bf16_f32 v30, v30, v31
	v_cvt_pk_bf16_f32 v31, v32, v33
	v_xor_b32_e32 v32, v34, v179
	v_max_f32_e32 v29, 0, v29
	v_cvt_pk_bf16_f32 v26, v26, v27
	v_cvt_pk_bf16_f32 v27, v28, v29
	v_bitop3_b32 v28, v34, v179, 16 bitop3:0x1e
	v_add_f32_e32 v2, v2, v66
	v_lshlrev_b32_e32 v32, 4, v32
	v_lshlrev_b32_e32 v28, 4, v28
	v_add_f32_e32 v22, v22, v66
	v_add_f32_e32 v23, v23, v67
	v_add_f32_e32 v18, v18, v66
	v_add_f32_e32 v19, v19, v67
	v_add_f32_e32 v14, v14, v66
	v_add_f32_e32 v15, v15, v67
	v_add_f32_e32 v10, v10, v66
	v_add_f32_e32 v11, v11, v67
	v_add_f32_e32 v6, v6, v66
	v_add_f32_e32 v7, v7, v67
	v_max_f32_e32 v2, 0, v2
	v_add_f32_e32 v3, v3, v67
	v_add3_u32 v32, v103, v32, v102
	v_add3_u32 v28, v103, v28, v102
	v_max_f32_e32 v22, 0, v22
	v_max_f32_e32 v23, 0, v23
	v_add_f32_e32 v24, v24, v68
	v_add_f32_e32 v25, v25, v69
	v_max_f32_e32 v18, 0, v18
	v_max_f32_e32 v19, 0, v19
	v_add_f32_e32 v20, v20, v68
	v_add_f32_e32 v21, v21, v69
	v_max_f32_e32 v14, 0, v14
	v_max_f32_e32 v15, 0, v15
	v_add_f32_e32 v16, v16, v68
	v_add_f32_e32 v17, v17, v69
	v_max_f32_e32 v10, 0, v10
	v_max_f32_e32 v11, 0, v11
	v_add_f32_e32 v12, v12, v68
	v_add_f32_e32 v13, v13, v69
	v_max_f32_e32 v6, 0, v6
	v_max_f32_e32 v7, 0, v7
	v_add_f32_e32 v8, v8, v68
	v_add_f32_e32 v9, v9, v69
	v_max_f32_e32 v3, 0, v3
	v_add_f32_e32 v4, v4, v68
	v_add_f32_e32 v5, v5, v69
	v_cvt_pk_bf16_f32 v2, v2, v3
	ds_write_b64 v32, v[30:31]
	ds_write_b64 v28, v[26:27] offset:8192
	v_max_f32_e32 v24, 0, v24
	v_max_f32_e32 v25, 0, v25
	v_cvt_pk_bf16_f32 v22, v22, v23
	v_cvt_pk_bf16_f32 v23, v24, v25
	ds_write_b64 v32, v[22:23] offset:16384
	v_max_f32_e32 v20, 0, v20
	v_max_f32_e32 v21, 0, v21
	v_cvt_pk_bf16_f32 v18, v18, v19
	v_cvt_pk_bf16_f32 v19, v20, v21
	ds_write_b64 v28, v[18:19] offset:24576
	v_max_f32_e32 v16, 0, v16
	v_max_f32_e32 v17, 0, v17
	v_cvt_pk_bf16_f32 v14, v14, v15
	v_cvt_pk_bf16_f32 v15, v16, v17
	ds_write_b64 v32, v[14:15] offset:32768
	v_max_f32_e32 v12, 0, v12
	v_max_f32_e32 v13, 0, v13
	v_cvt_pk_bf16_f32 v10, v10, v11
	v_cvt_pk_bf16_f32 v11, v12, v13
	ds_write_b64 v28, v[10:11] offset:40960
	v_max_f32_e32 v8, 0, v8
	v_max_f32_e32 v9, 0, v9
	v_cvt_pk_bf16_f32 v6, v6, v7
	v_cvt_pk_bf16_f32 v7, v8, v9
	ds_write_b64 v32, v[6:7] offset:49152
	v_max_f32_e32 v4, 0, v4
	v_max_f32_e32 v5, 0, v5
	v_cvt_pk_bf16_f32 v3, v4, v5
	ds_write_b64 v28, v[2:3] offset:57344
	v_and_b32_e32 v2, 0x1f0, v1
	v_lshrrev_b32_e32 v1, 5, v0
	v_xor_b32_e32 v4, v1, v0
	v_mov_b32_e32 v3, 0
	v_lshlrev_b32_e32 v4, 4, v4
	v_lshl_add_u64 v[12:13], s[4:5], 0, v[2:3]
	v_lshlrev_b32_e32 v2, 9, v1
	v_and_b32_e32 v16, 0x1f0, v4
	v_add3_u32 v2, 0, v2, v16
	s_waitcnt lgkmcnt(0)
	s_barrier
	ds_read_b128 v[4:7], v2
	v_lshlrev_b32_e32 v2, 11, v1
	v_lshl_add_u64 v[14:15], v[12:13], 0, v[2:3]
	v_or_b32_e32 v2, 0x200, v0
	v_lshrrev_b32_e32 v2, 5, v2
	v_xor_b32_e32 v9, v2, v0
	v_lshlrev_b32_e32 v9, 4, v9
	v_lshlrev_b32_e32 v8, 9, v2
	v_and_b32_e32 v9, 0x1f0, v9
	v_add3_u32 v8, 0, v8, v9
	ds_read_b128 v[8:11], v8
	v_lshlrev_b32_e32 v2, 11, v2
	s_waitcnt lgkmcnt(1)
	global_store_dwordx4 v[14:15], v[4:7], off sc1
	s_nop 1
	v_lshl_add_u64 v[4:5], v[12:13], 0, v[2:3]
	s_waitcnt lgkmcnt(0)
	global_store_dwordx4 v[4:5], v[8:11], off sc1
	v_or_b32_e32 v2, 32, v1
	v_lshlrev_b32_e32 v4, 9, v2
	v_or_b32_e32 v8, 0x600, v0
	v_lshrrev_b32_e32 v17, 5, v8
	v_xor_b32_e32 v9, v17, v0
	v_lshlrev_b32_e32 v9, 4, v9
	v_add3_u32 v4, 0, v4, v16
	v_lshlrev_b32_e32 v8, 9, v17
	v_and_b32_e32 v9, 0x1f0, v9
	ds_read_b128 v[4:7], v4
	v_add3_u32 v8, 0, v8, v9
	ds_read_b128 v[8:11], v8
	v_lshlrev_b32_e32 v2, 11, v2
	v_lshl_add_u64 v[14:15], v[12:13], 0, v[2:3]
	v_lshlrev_b32_e32 v2, 11, v17
	s_waitcnt lgkmcnt(1)
	global_store_dwordx4 v[14:15], v[4:7], off sc1
	s_nop 1
	v_lshl_add_u64 v[4:5], v[12:13], 0, v[2:3]
	s_waitcnt lgkmcnt(0)
	global_store_dwordx4 v[4:5], v[8:11], off sc1
	v_or_b32_e32 v2, 64, v1
	v_lshlrev_b32_e32 v4, 9, v2
	v_or_b32_e32 v8, 0xa00, v0
	v_lshrrev_b32_e32 v17, 5, v8
	v_xor_b32_e32 v9, v17, v0
	v_lshlrev_b32_e32 v9, 4, v9
	v_add3_u32 v4, 0, v4, v16
	v_lshlrev_b32_e32 v8, 9, v17
	v_and_b32_e32 v9, 0x1f0, v9
	ds_read_b128 v[4:7], v4
	v_add3_u32 v8, 0, v8, v9
	ds_read_b128 v[8:11], v8
	v_lshlrev_b32_e32 v2, 11, v2
	v_lshl_add_u64 v[14:15], v[12:13], 0, v[2:3]
	v_lshlrev_b32_e32 v2, 11, v17
	s_waitcnt lgkmcnt(1)
	global_store_dwordx4 v[14:15], v[4:7], off sc1
	s_nop 1
	v_lshl_add_u64 v[4:5], v[12:13], 0, v[2:3]
	s_waitcnt lgkmcnt(0)
	global_store_dwordx4 v[4:5], v[8:11], off sc1
	v_or_b32_e32 v2, 0x60, v1
	v_lshlrev_b32_e32 v4, 9, v2
	v_or_b32_e32 v8, 0xe00, v0
	v_lshrrev_b32_e32 v17, 5, v8
	v_xor_b32_e32 v9, v17, v0
	v_lshlrev_b32_e32 v9, 4, v9
	v_add3_u32 v4, 0, v4, v16
	v_lshlrev_b32_e32 v8, 9, v17
	v_and_b32_e32 v9, 0x1f0, v9
	ds_read_b128 v[4:7], v4
	v_add3_u32 v8, 0, v8, v9
	ds_read_b128 v[8:11], v8
	v_lshlrev_b32_e32 v2, 11, v2
	v_lshl_add_u64 v[14:15], v[12:13], 0, v[2:3]
	v_lshlrev_b32_e32 v2, 11, v17
	s_waitcnt lgkmcnt(1)
	global_store_dwordx4 v[14:15], v[4:7], off sc1
	s_nop 1
	v_lshl_add_u64 v[4:5], v[12:13], 0, v[2:3]
	s_waitcnt lgkmcnt(0)
	global_store_dwordx4 v[4:5], v[8:11], off sc1
	v_or_b32_e32 v2, 0x80, v1
	v_lshlrev_b32_e32 v4, 9, v2
	v_or_b32_e32 v8, 0x1200, v0
	v_lshrrev_b32_e32 v17, 5, v8
	v_xor_b32_e32 v9, v17, v0
	v_lshlrev_b32_e32 v9, 4, v9
	v_add3_u32 v4, 0, v4, v16
	v_lshlrev_b32_e32 v8, 9, v17
	v_and_b32_e32 v9, 0x1f0, v9
	ds_read_b128 v[4:7], v4
	v_add3_u32 v8, 0, v8, v9
	ds_read_b128 v[8:11], v8
	v_lshlrev_b32_e32 v2, 11, v2
	v_lshl_add_u64 v[14:15], v[12:13], 0, v[2:3]
	v_lshlrev_b32_e32 v2, 11, v17
	s_waitcnt lgkmcnt(1)
	global_store_dwordx4 v[14:15], v[4:7], off sc1
	s_nop 1
	v_lshl_add_u64 v[4:5], v[12:13], 0, v[2:3]
	s_waitcnt lgkmcnt(0)
	global_store_dwordx4 v[4:5], v[8:11], off sc1
	v_or_b32_e32 v2, 0xa0, v1
	v_lshlrev_b32_e32 v4, 9, v2
	v_or_b32_e32 v8, 0x1600, v0
	v_lshrrev_b32_e32 v17, 5, v8
	v_xor_b32_e32 v9, v17, v0
	v_lshlrev_b32_e32 v9, 4, v9
	v_add3_u32 v4, 0, v4, v16
	v_lshlrev_b32_e32 v8, 9, v17
	v_and_b32_e32 v9, 0x1f0, v9
	ds_read_b128 v[4:7], v4
	v_add3_u32 v8, 0, v8, v9
	ds_read_b128 v[8:11], v8
	v_lshlrev_b32_e32 v2, 11, v2
	v_lshl_add_u64 v[14:15], v[12:13], 0, v[2:3]
	v_lshlrev_b32_e32 v2, 11, v17
	s_waitcnt lgkmcnt(1)
	global_store_dwordx4 v[14:15], v[4:7], off sc1
	s_nop 1
	v_lshl_add_u64 v[4:5], v[12:13], 0, v[2:3]
	s_waitcnt lgkmcnt(0)
	global_store_dwordx4 v[4:5], v[8:11], off sc1
	v_or_b32_e32 v2, 0xc0, v1
	v_lshlrev_b32_e32 v4, 9, v2
	v_or_b32_e32 v8, 0x1a00, v0
	v_lshrrev_b32_e32 v17, 5, v8
	v_xor_b32_e32 v9, v17, v0
	v_add3_u32 v4, 0, v4, v16
	v_lshlrev_b32_e32 v9, 4, v9
	ds_read_b128 v[4:7], v4
	v_lshlrev_b32_e32 v8, 9, v17
	v_and_b32_e32 v9, 0x1f0, v9
	v_add3_u32 v8, 0, v8, v9
	ds_read_b128 v[8:11], v8
	v_lshlrev_b32_e32 v2, 11, v2
	v_lshl_add_u64 v[14:15], v[12:13], 0, v[2:3]
	v_lshlrev_b32_e32 v2, 11, v17
	v_or_b32_e32 v1, 0xe0, v1
	s_waitcnt lgkmcnt(1)
	global_store_dwordx4 v[14:15], v[4:7], off sc1
	s_nop 1
	v_lshl_add_u64 v[4:5], v[12:13], 0, v[2:3]
	v_lshlrev_b32_e32 v2, 9, v1
	v_add3_u32 v2, 0, v2, v16
	s_waitcnt lgkmcnt(0)
	global_store_dwordx4 v[4:5], v[8:11], off sc1
	ds_read_b128 v[4:7], v2
	v_lshlrev_b32_e32 v2, 11, v1
	v_or_b32_e32 v1, 0x1e00, v0
	v_lshrrev_b32_e32 v1, 5, v1
	v_xor_b32_e32 v9, v1, v0
	v_lshlrev_b32_e32 v9, 4, v9
	v_lshlrev_b32_e32 v8, 9, v1
	v_and_b32_e32 v9, 0x1f0, v9
	v_add3_u32 v8, 0, v8, v9
	ds_read_b128 v[8:11], v8
	v_lshl_add_u64 v[14:15], v[12:13], 0, v[2:3]
	v_lshlrev_b32_e32 v2, 11, v1
	s_waitcnt lgkmcnt(1)
	global_store_dwordx4 v[14:15], v[4:7], off sc1
	s_nop 1
	v_lshl_add_u64 v[4:5], v[12:13], 0, v[2:3]
	s_waitcnt lgkmcnt(0)
	global_store_dwordx4 v[4:5], v[8:11], off sc1
	s_waitcnt lgkmcnt(0)
	s_barrier
	s_lshl_b32 s3, s2, 3
	s_and_b32 s3, s3, 56
	s_ashr_i32 s17, s2, 5
	s_add_i32 s20, s3, s17
	s_ashr_i32 s21, s20, 31
	s_bfe_u32 s16, s2, 0x20003
	s_lshl_b64 s[4:5], s[20:21], 17
	s_lshl_b64 s[6:7], s[20:21], 19
	s_add_u32 s6, s12, s6
	s_addc_u32 s7, s13, s7
	s_lshl_b32 s3, s16, 19
	s_add_u32 s3, s14, s3
	v_ashrrev_i32_e32 v2, 6, v0
	v_lshlrev_b32_e32 v1, 4, v0
	s_addc_u32 s13, s15, 0
	v_lshlrev_b32_e32 v4, 9, v2
	v_and_b32_e32 v5, 0x1f0, v1
	s_add_u32 s12, s3, 0x400000
	v_and_or_b32 v32, v4, s0, v5
	v_lshlrev_b32_e32 v4, 5, v2
	v_and_b32_e32 v5, 48, v1
	s_addc_u32 s13, s13, 0
	v_bitop3_b32 v4, v4, v5, 32 bitop3:0x6c
	s_and_b32 s15, s2, 8
	s_add_i32 s3, s20, 3
	v_bfe_u32 v31, v0, 5, 1
	v_lshrrev_b32_e32 v34, 1, v4
	v_add_u32_e32 v4, s15, v2
	s_mov_b32 s20, 0x3ffffe
	v_and_or_b32 v30, v4, s20, v31
	v_bfe_i32 v5, v30, 0, 22
	v_bfe_u32 v4, v30, 21, 1
	v_add_u32_e32 v6, v5, v4
	v_lshlrev_b32_e32 v4, 3, v6
	v_and_b32_e32 v6, 0x7fffffe, v6
	s_lshl_b32 s0, s17, 4
	v_sub_u32_e32 v5, v5, v6
	s_and_b32 s17, s0, 16
	v_lshl_or_b32 v6, v5, 5, v34
	v_add_u32_e32 v5, s17, v2
	v_and_or_b32 v35, v5, s20, v31
	v_bfe_i32 v7, v35, 0, 22
	v_bfe_u32 v8, v35, 21, 1
	v_add_u32_e32 v8, v7, v8
	v_lshlrev_b32_e32 v9, 3, v8
	v_and_b32_e32 v8, 0x7fffffe, v8
	v_add_u32_e32 v5, 8, v5
	v_sub_u32_e32 v7, v7, v8
	v_and_or_b32 v36, v5, s20, v31
	v_lshl_or_b32 v98, v7, 5, v34
	v_bfe_i32 v5, v36, 0, 22
	v_bfe_u32 v7, v36, 21, 1
	v_add_u32_e32 v7, v5, v7
	v_lshrrev_b32_e32 v33, 6, v32
	v_lshlrev_b32_e32 v8, 3, v7
	v_and_b32_e32 v7, 0x7fffffe, v7
	s_and_b32 s3, s3, 15
	v_and_or_b32 v4, v4, -16, v33
	v_sub_u32_e32 v5, v5, v7
	v_and_or_b32 v14, v9, -16, v33
	v_lshl_or_b32 v100, v5, 5, v34
	v_ashrrev_i32_e32 v5, 31, v4
	s_lshl_b32 s14, s3, 6
	s_lshl_b32 s0, s3, 8
	s_lshl_b32 s2, s3, 7
	v_and_or_b32 v16, v8, -16, v33
	v_lshlrev_b64 v[4:5], 12, v[4:5]
	s_add_u32 s2, s12, s2
	v_ashrrev_i32_e32 v15, 31, v14
	v_lshl_add_u64 v[4:5], s[6:7], 0, v[4:5]
	v_ashrrev_i32_e32 v7, 31, v6
	s_addc_u32 s3, s13, 0
	v_lshlrev_b64 v[102:103], 11, v[14:15]
	v_ashrrev_i32_e32 v99, 31, v98
	v_ashrrev_i32_e32 v17, 31, v16
	v_lshl_add_u64 v[8:9], v[4:5], 0, s[0:1]
	v_lshlrev_b64 v[38:39], 2, v[6:7]
	v_lshl_add_u64 v[14:15], s[2:3], 0, v[102:103]
	v_lshlrev_b64 v[22:23], 1, v[98:99]
	v_lshlrev_b64 v[104:105], 11, v[16:17]
	v_ashrrev_i32_e32 v101, 31, v100
	v_lshl_add_u64 v[18:19], v[8:9], 0, v[38:39]
	v_lshl_add_u64 v[24:25], v[14:15], 0, v[22:23]
	v_lshl_add_u64 v[14:15], s[2:3], 0, v[104:105]
	v_lshlrev_b64 v[26:27], 1, v[100:101]
	global_load_dwordx4 v[6:9], v[18:19], off offset:16
	global_load_dwordx4 v[10:13], v[18:19], off
	v_lshl_add_u64 v[28:29], v[14:15], 0, v[26:27]
	global_load_dwordx4 v[14:17], v[24:25], off
	global_load_dwordx4 v[18:21], v[28:29], off
	v_lshlrev_b32_e32 v24, 10, v30
	v_or_b32_e32 v125, v24, v32
	v_xad_u32 v24, s15, 8, v2
	v_and_or_b32 v24, v24, s20, v31
	v_lshlrev_b32_e32 v25, 10, v24
	v_or_b32_e32 v122, v25, v32
	v_bfe_i32 v25, v24, 0, 22
	v_bfe_u32 v24, v24, 21, 1
	v_add_u32_e32 v28, v25, v24
	v_lshlrev_b32_e32 v24, 3, v28
	v_and_b32_e32 v28, 0x7fffffe, v28
	v_sub_u32_e32 v25, v25, v28
	v_lshl_or_b32 v28, v25, 5, v34
	v_lshlrev_b32_e32 v25, 10, v35
	v_or_b32_e32 v126, v25, v32
	v_lshlrev_b32_e32 v25, 10, v36
	v_or_b32_e32 v127, v25, v32
	v_xad_u32 v25, s17, 16, v2
	v_and_or_b32 v25, v25, s20, v31
	v_lshlrev_b32_e32 v29, 10, v25
	v_or_b32_e32 v123, v29, v32
	v_bfe_i32 v29, v25, 0, 22
	v_bfe_u32 v25, v25, 21, 1
	v_add_u32_e32 v25, v29, v25
	v_and_b32_e32 v121, 3, v2
	v_lshlrev_b32_e32 v30, 3, v25
	v_and_b32_e32 v25, 0x7fffffe, v25
	v_xad_u32 v2, s17, 24, v2
	v_sub_u32_e32 v25, v29, v25
	v_and_or_b32 v2, v2, s20, v31
	v_lshl_or_b32 v106, v25, 5, v34
	v_lshlrev_b32_e32 v25, 10, v2
	v_or_b32_e32 v124, v25, v32
	v_bfe_i32 v25, v2, 0, 22
	v_bfe_u32 v2, v2, 21, 1
	v_add_u32_e32 v2, v25, v2
	v_lshlrev_b32_e32 v29, 3, v2
	v_and_b32_e32 v2, 0x7fffffe, v2
	v_and_b32_e32 v118, 15, v0
	v_sub_u32_e32 v2, v25, v2
	v_lshlrev_b32_e32 v25, 2, v0
	v_ashrrev_i32_e32 v120, 8, v0
	v_and_or_b32 v32, v29, -16, v33
	v_lshl_or_b32 v108, v2, 5, v34
	v_and_b32_e32 v2, 48, v0
	v_and_b32_e32 v25, 32, v25
	v_lshlrev_b32_e32 v29, 6, v118
	v_and_b32_e32 v119, 63, v0
	v_and_or_b32 v24, v24, -16, v33
	v_and_or_b32 v30, v30, -16, v33
	v_lshlrev_b32_e32 v68, 13, v120
	v_bitop3_b32 v2, v29, v25, v2 bitop3:0x36
	v_ashrrev_i32_e32 v25, 31, v24
	v_lshlrev_b64 v[24:25], 12, v[24:25]
	v_lshl_add_u64 v[56:57], s[6:7], 0, v[24:25]
	v_ashrrev_i32_e32 v29, 31, v28
	v_lshl_add_u64 v[24:25], v[56:57], 0, s[0:1]
	v_lshlrev_b64 v[58:59], 2, v[28:29]
	v_ashrrev_i32_e32 v31, 31, v30
	v_lshl_add_u64 v[24:25], v[24:25], 0, v[58:59]
	v_lshlrev_b64 v[110:111], 11, v[30:31]
	v_ashrrev_i32_e32 v107, 31, v106
	v_ashrrev_i32_e32 v33, 31, v32
	global_load_dwordx4 v[40:43], v[24:25], off offset:16
	global_load_dwordx4 v[44:47], v[24:25], off
	v_lshl_add_u64 v[24:25], s[2:3], 0, v[110:111]
	v_lshlrev_b64 v[60:61], 1, v[106:107]
	v_lshlrev_b64 v[112:113], 11, v[32:33]
	v_ashrrev_i32_e32 v109, 31, v108
	v_lshl_add_u64 v[24:25], v[24:25], 0, v[60:61]
	v_lshl_add_u64 v[28:29], s[2:3], 0, v[112:113]
	v_lshlrev_b64 v[62:63], 1, v[108:109]
	v_lshl_add_u64 v[28:29], v[28:29], 0, v[62:63]
	global_load_dwordx4 v[48:51], v[24:25], off
	global_load_dwordx4 v[52:55], v[28:29], off
	s_add_i32 s0, s14, 64
	s_and_b32 s2, s0, 0x3c0
	s_lshl_b32 s0, s2, 2
	s_lshl_b32 s2, s2, 1
	v_lshl_add_u64 v[24:25], v[4:5], 0, s[0:1]
	s_add_u32 s2, s12, s2
	v_lshl_add_u64 v[24:25], v[24:25], 0, v[38:39]
	s_addc_u32 s3, s13, 0
	global_load_dwordx4 v[30:33], v[24:25], off offset:16
	global_load_dwordx4 v[34:37], v[24:25], off
	v_lshl_add_u64 v[24:25], s[2:3], 0, v[102:103]
	v_lshl_add_u64 v[64:65], v[24:25], 0, v[22:23]
	v_lshl_add_u64 v[22:23], s[2:3], 0, v[104:105]
	v_lshl_add_u64 v[66:67], v[22:23], 0, v[26:27]
	global_load_dwordx4 v[26:29], v[64:65], off
	global_load_dwordx4 v[22:25], v[66:67], off
	v_add_u32_e32 v64, 0, v125
	s_waitcnt vmcnt(10)
	v_cvt_pk_bf16_f32 v10, v10, v11
	v_cvt_pk_bf16_f32 v11, v12, v13
	v_cvt_pk_bf16_f32 v12, v6, v7
	v_add_u32_e32 v6, 0, v126
	v_cvt_pk_bf16_f32 v13, v8, v9
	ds_write_b128 v64, v[10:13]
	s_waitcnt vmcnt(9)
	ds_write_b128 v6, v[14:17] offset:32768
	v_add_u32_e32 v6, 0, v127
	s_waitcnt vmcnt(8)
	ds_write_b128 v6, v[18:21] offset:32768
	v_add_u32_e32 v10, 0, v122
	s_waitcnt vmcnt(6)
	v_cvt_pk_bf16_f32 v6, v44, v45
	v_cvt_pk_bf16_f32 v7, v46, v47
	v_cvt_pk_bf16_f32 v8, v40, v41
	v_cvt_pk_bf16_f32 v9, v42, v43
	ds_write_b128 v10, v[6:9]
	v_add_u32_e32 v6, 0, v123
	s_waitcnt vmcnt(5)
	ds_write_b128 v6, v[48:51] offset:32768
	v_add_u32_e32 v6, 0, v124
	s_waitcnt vmcnt(4)
	ds_write_b128 v6, v[52:55] offset:32768
	v_lshl_add_u64 v[6:7], v[56:57], 0, s[0:1]
	v_lshl_add_u64 v[14:15], v[6:7], 0, v[58:59]
	global_load_dwordx4 v[6:9], v[14:15], off offset:16
	global_load_dwordx4 v[10:13], v[14:15], off
	v_lshl_add_u64 v[14:15], s[2:3], 0, v[110:111]
	v_lshl_add_u64 v[40:41], v[14:15], 0, v[60:61]
	v_lshl_add_u64 v[14:15], s[2:3], 0, v[112:113]
	v_lshl_add_u64 v[42:43], v[14:15], 0, v[62:63]
	global_load_dwordx4 v[18:21], v[40:41], off
	global_load_dwordx4 v[14:17], v[42:43], off
	v_lshlrev_b32_e32 v40, 13, v121
	s_cmp_lg_u32 0, -1
	s_waitcnt lgkmcnt(0)
	s_cselect_b32 s0, 0, 0
	v_add3_u32 v128, v68, s0, v2
	s_add_i32 s0, s0, 0x8000
	v_add3_u32 v129, v40, s0, v2
	v_lshl_add_u64 v[114:115], v[4:5], 0, v[38:39]
	v_lshl_add_u64 v[116:117], v[56:57], 0, v[58:59]
	s_add_i32 s2, s14, 0x80
	s_mov_b32 s3, 0
	v_mov_b32_e32 v2, v3
	v_mov_b32_e32 v4, v3
	v_mov_b32_e32 v5, v3
	v_mov_b32_e32 v38, v3
	v_mov_b32_e32 v39, v3
	v_mov_b32_e32 v40, v3
	v_mov_b32_e32 v41, v3
	v_mov_b32_e32 v42, v3
	v_mov_b32_e32 v43, v3
	v_mov_b32_e32 v44, v3
	v_mov_b32_e32 v45, v3
	v_mov_b32_e32 v46, v3
	v_mov_b32_e32 v47, v3
	v_mov_b32_e32 v48, v3
	v_mov_b32_e32 v49, v3
	v_mov_b32_e32 v50, v3
	v_mov_b32_e32 v51, v3
	v_mov_b32_e32 v52, v3
	v_mov_b32_e32 v53, v3
	v_mov_b32_e32 v54, v3
	v_mov_b32_e32 v55, v3
	v_mov_b32_e32 v56, v3
	v_mov_b32_e32 v57, v3
	v_mov_b32_e32 v58, v3
	v_mov_b32_e32 v59, v3
	v_mov_b32_e32 v60, v3
	v_mov_b32_e32 v61, v3
	v_mov_b32_e32 v62, v3
	v_mov_b32_e32 v63, v3
	v_mov_b32_e32 v64, v3
	v_mov_b32_e32 v65, v3
	v_mov_b32_e32 v66, v3
	v_mov_b32_e32 v67, v3
	v_mov_b32_e32 v68, v3
	v_mov_b32_e32 v69, v3
	v_mov_b32_e32 v70, v3
	v_mov_b32_e32 v71, v3
	v_mov_b32_e32 v72, v3
	v_mov_b32_e32 v73, v3
	v_mov_b32_e32 v74, v3
	v_mov_b32_e32 v75, v3
	v_mov_b32_e32 v76, v3
	v_mov_b32_e32 v77, v3
	v_mov_b32_e32 v78, v3
	v_mov_b32_e32 v79, v3
	v_mov_b32_e32 v80, v3
	v_mov_b32_e32 v81, v3
	v_mov_b32_e32 v82, v3
	v_mov_b32_e32 v83, v3
	v_mov_b32_e32 v84, v3
	v_mov_b32_e32 v85, v3
	v_mov_b32_e32 v86, v3
	v_mov_b32_e32 v87, v3
	v_mov_b32_e32 v88, v3
	v_mov_b32_e32 v89, v3
	v_mov_b32_e32 v90, v3
	v_mov_b32_e32 v91, v3
	v_mov_b32_e32 v92, v3
	v_mov_b32_e32 v93, v3
	v_mov_b32_e32 v94, v3
	v_mov_b32_e32 v95, v3
	v_mov_b32_e32 v96, v3
	v_mov_b32_e32 v97, v3
	s_barrier
	s_cmp_lg_u32 s40, 0
	s_cbranch_scc1 .Lrot2_loop

.Lrot2_done:
	ds_read_b128 v[98:101], v129 offset:0
	ds_read_b128 v[102:105], v129 offset:0x800
	ds_read_b128 v[106:109], v129 offset:0x1000
	ds_read_b128 v[110:113], v129 offset:0x1800
	ds_read_b128 v[114:117], v128 offset:0
	ds_read_b128 v[130:133], v128 offset:0x800
	ds_read_b128 v[134:137], v128 offset:0x1000
	s_nop 0
	s_waitcnt lgkmcnt(2)
	s_nop 0
	v_mfma_f32_16x16x32_bf16 v[94:97], v[98:101], v[114:117], v[94:97]
	v_mfma_f32_16x16x32_bf16 v[90:93], v[102:105], v[114:117], v[90:93]
	v_mfma_f32_16x16x32_bf16 v[86:89], v[106:109], v[114:117], v[86:89]
	v_mfma_f32_16x16x32_bf16 v[82:85], v[110:113], v[114:117], v[82:85]
	ds_read_b128 v[114:117], v128 offset:0x1800
	s_waitcnt lgkmcnt(2)
	s_nop 0
	v_mfma_f32_16x16x32_bf16 v[78:81], v[98:101], v[130:133], v[78:81]
	v_mfma_f32_16x16x32_bf16 v[74:77], v[102:105], v[130:133], v[74:77]
	v_mfma_f32_16x16x32_bf16 v[70:73], v[106:109], v[130:133], v[70:73]
	v_mfma_f32_16x16x32_bf16 v[66:69], v[110:113], v[130:133], v[66:69]
	s_waitcnt lgkmcnt(1)
	s_nop 0
	v_mfma_f32_16x16x32_bf16 v[62:65], v[98:101], v[134:137], v[62:65]
	v_mfma_f32_16x16x32_bf16 v[58:61], v[102:105], v[134:137], v[58:61]
	v_mfma_f32_16x16x32_bf16 v[54:57], v[106:109], v[134:137], v[54:57]
	v_mfma_f32_16x16x32_bf16 v[50:53], v[110:113], v[134:137], v[50:53]
	s_waitcnt lgkmcnt(0)
	s_nop 0
	v_mfma_f32_16x16x32_bf16 v[46:49], v[98:101], v[114:117], v[46:49]
	v_mfma_f32_16x16x32_bf16 v[42:45], v[102:105], v[114:117], v[42:45]
	v_mfma_f32_16x16x32_bf16 v[38:41], v[106:109], v[114:117], v[38:41]
	v_mfma_f32_16x16x32_bf16 v[2:5], v[110:113], v[114:117], v[2:5]
	v_add_u32_e32 v98, s18, v125
	s_waitcnt vmcnt(6)
	v_cvt_pk_bf16_f32 v34, v34, v35
	v_cvt_pk_bf16_f32 v35, v36, v37
	v_cvt_pk_bf16_f32 v36, v30, v31
	v_add_u32_e32 v30, s19, v126
	v_cvt_pk_bf16_f32 v37, v32, v33
	ds_write_b128 v98, v[34:37]
	s_waitcnt vmcnt(5)
	ds_write_b128 v30, v[26:29]
	v_add_u32_e32 v26, s19, v127
	s_waitcnt vmcnt(4)
	ds_write_b128 v26, v[22:25]
	ds_read_b128 v[22:25], v129 offset:0x400
	ds_read_b128 v[26:29], v129 offset:0xc00
	ds_read_b128 v[30:33], v129 offset:0x1400
	ds_read_b128 v[34:37], v129 offset:0x1c00
	ds_read_b128 v[98:101], v128 offset:0x400
	ds_read_b128 v[102:105], v128 offset:0xc00
	ds_read_b128 v[106:109], v128 offset:0x1400
	s_nop 0
	s_waitcnt lgkmcnt(2)
	s_nop 0
	v_mfma_f32_16x16x32_bf16 v[94:97], v[22:25], v[98:101], v[94:97]
	v_mfma_f32_16x16x32_bf16 v[90:93], v[26:29], v[98:101], v[90:93]
	v_mfma_f32_16x16x32_bf16 v[86:89], v[30:33], v[98:101], v[86:89]
	v_mfma_f32_16x16x32_bf16 v[82:85], v[34:37], v[98:101], v[82:85]
	ds_read_b128 v[98:101], v128 offset:0x1c00
	s_waitcnt lgkmcnt(2)
	s_nop 0
	v_mfma_f32_16x16x32_bf16 v[78:81], v[22:25], v[102:105], v[78:81]
	v_mfma_f32_16x16x32_bf16 v[74:77], v[26:29], v[102:105], v[74:77]
	v_mfma_f32_16x16x32_bf16 v[70:73], v[30:33], v[102:105], v[70:73]
	v_mfma_f32_16x16x32_bf16 v[66:69], v[34:37], v[102:105], v[66:69]
	s_waitcnt lgkmcnt(1)
	s_nop 0
	v_mfma_f32_16x16x32_bf16 v[62:65], v[22:25], v[106:109], v[62:65]
	v_mfma_f32_16x16x32_bf16 v[58:61], v[26:29], v[106:109], v[58:61]
	v_mfma_f32_16x16x32_bf16 v[54:57], v[30:33], v[106:109], v[54:57]
	v_mfma_f32_16x16x32_bf16 v[50:53], v[34:37], v[106:109], v[50:53]
	s_waitcnt lgkmcnt(0)
	s_nop 0
	v_mfma_f32_16x16x32_bf16 v[22:25], v[22:25], v[98:101], v[46:49]
	v_mfma_f32_16x16x32_bf16 v[26:29], v[26:29], v[98:101], v[42:45]
	v_mfma_f32_16x16x32_bf16 v[30:33], v[30:33], v[98:101], v[38:41]
	v_mfma_f32_16x16x32_bf16 v[2:5], v[34:37], v[98:101], v[2:5]
	v_add_u32_e32 v34, s18, v122
	s_waitcnt vmcnt(2)
	v_cvt_pk_bf16_f32 v10, v10, v11
	v_cvt_pk_bf16_f32 v11, v12, v13
	v_cvt_pk_bf16_f32 v12, v6, v7
	v_add_u32_e32 v6, s19, v123
	s_lshl_b64 s[0:1], s[4:5], 1
	v_cvt_pk_bf16_f32 v13, v8, v9
	ds_write_b128 v34, v[10:13]
	s_waitcnt vmcnt(1)
	ds_write_b128 v6, v[18:21]
	v_add_u32_e32 v6, s19, v124
	s_add_u32 s0, s10, s0
	s_waitcnt vmcnt(0)
	ds_write_b128 v6, v[14:17]
	s_addc_u32 s1, s11, s1
	s_lshl_b32 s2, s16, 9
	s_waitcnt lgkmcnt(0)
	s_barrier
	v_add_u32_e32 v110, 0x10000, v128
	v_add_u32_e32 v102, 0x10000, v129
	ds_read_b128 v[6:9], v102 offset:0
	ds_read_b128 v[10:13], v102 offset:0x800
	ds_read_b128 v[14:17], v102 offset:0x1000
	ds_read_b128 v[18:21], v102 offset:0x1800
	ds_read_b128 v[34:37], v110 offset:0
	ds_read_b128 v[38:41], v110 offset:0x800
	ds_read_b128 v[42:45], v110 offset:0x1000
	s_add_u32 s0, s0, s2
	s_addc_u32 s1, s1, 0
	s_lshl_b32 s2, s16, 10
	s_waitcnt lgkmcnt(2)
	s_add_u32 s2, s8, s2
	v_mfma_f32_16x16x32_bf16 v[46:49], v[6:9], v[34:37], v[94:97]
	s_addc_u32 s3, s9, 0
	v_mfma_f32_16x16x32_bf16 v[90:93], v[10:13], v[34:37], v[90:93]
	v_mfma_f32_16x16x32_bf16 v[86:89], v[14:17], v[34:37], v[86:89]
	v_mfma_f32_16x16x32_bf16 v[34:37], v[18:21], v[34:37], v[82:85]
	ds_read_b128 v[82:85], v110 offset:0x1800
	s_waitcnt lgkmcnt(2)
	s_nop 0
	v_mfma_f32_16x16x32_bf16 v[78:81], v[6:9], v[38:41], v[78:81]
	v_mfma_f32_16x16x32_bf16 v[74:77], v[10:13], v[38:41], v[74:77]
	v_mfma_f32_16x16x32_bf16 v[70:73], v[14:17], v[38:41], v[70:73]
	v_mfma_f32_16x16x32_bf16 v[38:41], v[18:21], v[38:41], v[66:69]
	s_waitcnt lgkmcnt(1)
	s_nop 0
	v_mfma_f32_16x16x32_bf16 v[62:65], v[6:9], v[42:45], v[62:65]
	v_mfma_f32_16x16x32_bf16 v[58:61], v[10:13], v[42:45], v[58:61]
	v_mfma_f32_16x16x32_bf16 v[54:57], v[14:17], v[42:45], v[54:57]
	v_mfma_f32_16x16x32_bf16 v[42:45], v[18:21], v[42:45], v[50:53]
	s_waitcnt lgkmcnt(0)
	s_nop 0
	v_mfma_f32_16x16x32_bf16 v[50:53], v[6:9], v[82:85], v[22:25]
	v_mfma_f32_16x16x32_bf16 v[66:69], v[10:13], v[82:85], v[26:29]
	v_mfma_f32_16x16x32_bf16 v[94:97], v[14:17], v[82:85], v[30:33]
	v_mfma_f32_16x16x32_bf16 v[2:5], v[18:21], v[82:85], v[2:5]
	ds_read_b128 v[18:21], v102 offset:0x400
	ds_read_b128 v[82:85], v102 offset:0xc00
	ds_read_b128 v[98:101], v102 offset:0x1400
	ds_read_b128 v[102:105], v102 offset:0x1c00
	ds_read_b128 v[6:9], v110 offset:0x400
	ds_read_b128 v[10:13], v110 offset:0xc00
	ds_read_b128 v[106:109], v110 offset:0x1400
	s_nop 0
	s_waitcnt lgkmcnt(2)
	s_nop 0
	v_mfma_f32_16x16x32_bf16 v[46:49], v[18:21], v[6:9], v[46:49]
	v_mfma_f32_16x16x32_bf16 v[90:93], v[82:85], v[6:9], v[90:93]
	v_mfma_f32_16x16x32_bf16 v[30:33], v[98:101], v[6:9], v[86:89]
	v_mfma_f32_16x16x32_bf16 v[14:17], v[102:105], v[6:9], v[34:37]
	ds_read_b128 v[86:89], v110 offset:0x1c00
	s_waitcnt lgkmcnt(2)
	s_nop 0
	v_mfma_f32_16x16x32_bf16 v[78:81], v[18:21], v[10:13], v[78:81]
	v_mfma_f32_16x16x32_bf16 v[74:77], v[82:85], v[10:13], v[74:77]
	v_mfma_f32_16x16x32_bf16 v[26:29], v[98:101], v[10:13], v[70:73]
	v_mfma_f32_16x16x32_bf16 v[10:13], v[102:105], v[10:13], v[38:41]
	s_waitcnt lgkmcnt(1)
	s_nop 0
	v_mfma_f32_16x16x32_bf16 v[62:65], v[18:21], v[106:109], v[62:65]
	v_mfma_f32_16x16x32_bf16 v[38:41], v[82:85], v[106:109], v[58:61]
	v_mfma_f32_16x16x32_bf16 v[22:25], v[98:101], v[106:109], v[54:57]
	v_mfma_f32_16x16x32_bf16 v[6:9], v[102:105], v[106:109], v[42:45]
	s_waitcnt lgkmcnt(0)
	s_nop 0
	v_mfma_f32_16x16x32_bf16 v[42:45], v[18:21], v[86:89], v[50:53]
	v_mfma_f32_16x16x32_bf16 v[34:37], v[82:85], v[86:89], v[66:69]
	v_mfma_f32_16x16x32_bf16 v[18:21], v[98:101], v[86:89], v[94:97]
	v_mfma_f32_16x16x32_bf16 v[2:5], v[102:105], v[86:89], v[2:5]
	v_lshrrev_b32_e32 v50, 2, v119
	v_and_b32_e32 v50, 12, v50
	v_lshl_or_b32 v66, v121, 6, v50
	v_lshlrev_b32_e32 v67, 2, v66
	s_waitcnt lgkmcnt(0)
	s_barrier
	global_load_dwordx4 v[50:53], v67, s[2:3]
	global_load_dwordx4 v[54:57], v67, s[2:3] offset:64
	v_lshrrev_b32_e32 v58, 1, v119
	v_lshl_or_b32 v59, v120, 6, v118
	v_and_b32_e32 v68, 8, v58
	v_lshl_add_u32 v69, v59, 9, 0
	v_or_b32_e32 v70, 16, v59
	v_or_b32_e32 v71, 48, v59
	v_lshrrev_b32_e32 v58, 3, v66
	v_or_b32_e32 v59, 16, v66
	v_bitop3_b32 v83, v70, v58, 31 bitop3:0x6c
	v_lshrrev_b32_e32 v85, 3, v59
	v_lshl_add_u32 v72, v70, 9, 0
	v_xor_b32_e32 v82, v58, v118
	v_bitop3_b32 v84, v71, v58, 31 bitop3:0x6c
	v_lshlrev_b32_e32 v83, 4, v83
	v_xor_b32_e32 v86, v85, v118
	v_lshl_add_u32 v73, v71, 9, 0
	v_lshlrev_b32_e32 v82, 4, v82
	v_lshlrev_b32_e32 v84, 4, v84
	v_add3_u32 v83, v72, v83, v68
	v_lshlrev_b32_e32 v86, 4, v86
	global_load_dwordx4 v[58:61], v67, s[2:3] offset:128
	v_add3_u32 v82, v69, v82, v68
	v_add3_u32 v84, v73, v84, v68
	v_add3_u32 v86, v69, v86, v68
	s_waitcnt vmcnt(2)
	v_add_f32_e32 v46, v46, v50
	v_add_f32_e32 v47, v47, v51
	v_add_f32_e32 v48, v48, v52
	v_add_f32_e32 v49, v49, v53
	v_add_f32_e32 v78, v78, v50
	v_add_f32_e32 v79, v79, v51
	v_add_f32_e32 v80, v80, v52
	v_add_f32_e32 v81, v81, v53
	v_add_f32_e32 v62, v62, v50
	v_add_f32_e32 v63, v63, v51
	v_add_f32_e32 v42, v42, v50
	v_add_f32_e32 v43, v43, v51
	v_add_f32_e32 v44, v44, v52
	v_add_f32_e32 v45, v45, v53
	s_waitcnt vmcnt(1)
	v_add_f32_e32 v50, v90, v54
	v_add_f32_e32 v51, v91, v55
	v_add_f32_e32 v64, v64, v52
	v_add_f32_e32 v65, v65, v53
	v_add_f32_e32 v52, v92, v56
	v_add_f32_e32 v53, v93, v57
	v_max_f32_e32 v46, 0, v46
	v_max_f32_e32 v47, 0, v47
	v_max_f32_e32 v48, 0, v48
	v_max_f32_e32 v49, 0, v49
	v_max_f32_e32 v78, 0, v78
	v_max_f32_e32 v79, 0, v79
	v_max_f32_e32 v80, 0, v80
	v_max_f32_e32 v81, 0, v81
	v_max_f32_e32 v88, 0, v43
	v_max_f32_e32 v89, 0, v44
	v_max_f32_e32 v90, 0, v45
	v_max_f32_e32 v50, 0, v50
	v_max_f32_e32 v51, 0, v51
	v_cvt_pk_bf16_f32 v43, v48, v49
	v_cvt_pk_bf16_f32 v44, v78, v79
	v_cvt_pk_bf16_f32 v45, v80, v81
	v_max_f32_e32 v62, 0, v62
	v_max_f32_e32 v63, 0, v63
	v_max_f32_e32 v64, 0, v64
	v_max_f32_e32 v65, 0, v65
	v_max_f32_e32 v87, 0, v42
	v_max_f32_e32 v52, 0, v52
	v_max_f32_e32 v53, 0, v53
	v_cvt_pk_bf16_f32 v42, v46, v47
	v_cvt_pk_bf16_f32 v46, v62, v63
	v_cvt_pk_bf16_f32 v47, v64, v65
	v_cvt_pk_bf16_f32 v48, v87, v88
	v_cvt_pk_bf16_f32 v49, v89, v90
	v_cvt_pk_bf16_f32 v50, v50, v51
	v_cvt_pk_bf16_f32 v51, v52, v53
	ds_write_b64 v83, v[44:45]
	ds_write2st64_b64 v82, v[42:43], v[46:47] offset1:32
	ds_write_b64 v84, v[48:49]
	ds_write_b64 v86, v[50:51]
	v_add_f32_e32 v43, v76, v56
	v_add_f32_e32 v44, v77, v57
	v_max_f32_e32 v43, 0, v43
	v_max_f32_e32 v44, 0, v44
	v_add_f32_e32 v42, v75, v55
	v_cvt_pk_bf16_f32 v43, v43, v44
	v_bitop3_b32 v44, v85, v70, 31 bitop3:0x78
	v_add_f32_e32 v74, v74, v54
	v_max_f32_e32 v42, 0, v42
	v_lshlrev_b32_e32 v44, 4, v44
	v_max_f32_e32 v74, 0, v74
	v_cvt_pk_bf16_f32 v42, v74, v42
	v_add3_u32 v44, v72, v44, v68
	ds_write_b64 v44, v[42:43]
	global_load_dwordx4 v[42:45], v67, s[2:3] offset:192
	v_add_f32_e32 v34, v34, v54
	v_add_f32_e32 v35, v35, v55
	v_add_f32_e32 v36, v36, v56
	v_max_f32_e32 v34, 0, v34
	v_max_f32_e32 v35, 0, v35
	v_max_f32_e32 v36, 0, v36
	v_add_f32_e32 v37, v37, v57
	v_max_f32_e32 v37, 0, v37
	v_cvt_pk_bf16_f32 v34, v34, v35
	v_cvt_pk_bf16_f32 v35, v36, v37
	v_bitop3_b32 v36, v85, v71, 31 bitop3:0x78
	v_add_f32_e32 v38, v38, v54
	v_add_f32_e32 v39, v39, v55
	v_lshlrev_b32_e32 v36, 4, v36
	v_max_f32_e32 v38, 0, v38
	v_max_f32_e32 v39, 0, v39
	v_add_f32_e32 v40, v40, v56
	v_add_f32_e32 v41, v41, v57
	v_add3_u32 v36, v73, v36, v68
	v_max_f32_e32 v40, 0, v40
	v_max_f32_e32 v41, 0, v41
	v_cvt_pk_bf16_f32 v38, v38, v39
	v_cvt_pk_bf16_f32 v39, v40, v41
	ds_write_b64 v86, v[38:39] offset:16384
	ds_write_b64 v36, v[34:35]
	v_or_b32_e32 v34, 32, v66
	s_waitcnt vmcnt(1)
	v_add_f32_e32 v30, v30, v58
	v_add_f32_e32 v31, v31, v59
	v_add_f32_e32 v32, v32, v60
	v_add_f32_e32 v26, v26, v58
	v_add_f32_e32 v27, v27, v59
	v_add_f32_e32 v28, v28, v60
	v_add_f32_e32 v18, v18, v58
	v_add_f32_e32 v19, v19, v59
	v_add_f32_e32 v20, v20, v60
	v_lshrrev_b32_e32 v34, 3, v34
	v_max_f32_e32 v30, 0, v30
	v_max_f32_e32 v31, 0, v31
	v_max_f32_e32 v32, 0, v32
	v_add_f32_e32 v33, v33, v61
	v_max_f32_e32 v26, 0, v26
	v_max_f32_e32 v27, 0, v27
	v_max_f32_e32 v28, 0, v28
	v_add_f32_e32 v29, v29, v61
	v_max_f32_e32 v18, 0, v18
	v_max_f32_e32 v19, 0, v19
	v_max_f32_e32 v20, 0, v20
	v_add_f32_e32 v21, v21, v61
	v_max_f32_e32 v33, 0, v33
	v_cvt_pk_bf16_f32 v30, v30, v31
	v_cvt_pk_bf16_f32 v31, v32, v33
	v_xor_b32_e32 v32, v34, v118
	v_max_f32_e32 v29, 0, v29
	v_cvt_pk_bf16_f32 v26, v26, v27
	v_cvt_pk_bf16_f32 v27, v28, v29
	v_bitop3_b32 v28, v34, v70, 31 bitop3:0x78
	v_max_f32_e32 v21, 0, v21
	v_cvt_pk_bf16_f32 v18, v18, v19
	v_cvt_pk_bf16_f32 v19, v20, v21
	v_bitop3_b32 v20, v34, v71, 31 bitop3:0x78
	v_lshlrev_b32_e32 v32, 4, v32
	v_lshlrev_b32_e32 v28, 4, v28
	v_add_f32_e32 v22, v22, v58
	v_add_f32_e32 v23, v23, v59
	v_lshlrev_b32_e32 v20, 4, v20
	v_add3_u32 v32, v69, v32, v68
	v_add3_u32 v28, v72, v28, v68
	v_max_f32_e32 v22, 0, v22
	v_max_f32_e32 v23, 0, v23
	v_add_f32_e32 v24, v24, v60
	v_add_f32_e32 v25, v25, v61
	v_add3_u32 v20, v73, v20, v68
	ds_write_b64 v32, v[30:31]
	ds_write_b64 v28, v[26:27]
	v_max_f32_e32 v24, 0, v24
	v_max_f32_e32 v25, 0, v25
	v_cvt_pk_bf16_f32 v22, v22, v23
	v_cvt_pk_bf16_f32 v23, v24, v25
	ds_write_b64 v32, v[22:23] offset:16384
	ds_write_b64 v20, v[18:19]
	v_or_b32_e32 v18, 48, v66
	s_waitcnt vmcnt(0)
	v_add_f32_e32 v14, v14, v42
	v_add_f32_e32 v15, v15, v43
	v_add_f32_e32 v16, v16, v44
	v_add_f32_e32 v10, v10, v42
	v_add_f32_e32 v11, v11, v43
	v_add_f32_e32 v12, v12, v44
	v_add_f32_e32 v2, v2, v42
	v_add_f32_e32 v3, v3, v43
	v_add_f32_e32 v4, v4, v44
	v_lshrrev_b32_e32 v18, 3, v18
	v_max_f32_e32 v14, 0, v14
	v_max_f32_e32 v15, 0, v15
	v_max_f32_e32 v16, 0, v16
	v_add_f32_e32 v17, v17, v45
	v_max_f32_e32 v10, 0, v10
	v_max_f32_e32 v11, 0, v11
	v_max_f32_e32 v12, 0, v12
	v_add_f32_e32 v13, v13, v45
	v_max_f32_e32 v2, 0, v2
	v_max_f32_e32 v3, 0, v3
	v_max_f32_e32 v4, 0, v4
	v_add_f32_e32 v5, v5, v45
	v_max_f32_e32 v17, 0, v17
	v_cvt_pk_bf16_f32 v14, v14, v15
	v_cvt_pk_bf16_f32 v15, v16, v17
	v_xor_b32_e32 v16, v18, v118
	v_max_f32_e32 v13, 0, v13
	v_cvt_pk_bf16_f32 v10, v10, v11
	v_cvt_pk_bf16_f32 v11, v12, v13
	v_bitop3_b32 v12, v18, v70, 31 bitop3:0x78
	v_max_f32_e32 v5, 0, v5
	v_cvt_pk_bf16_f32 v2, v2, v3
	v_cvt_pk_bf16_f32 v3, v4, v5
	v_bitop3_b32 v4, v18, v71, 31 bitop3:0x78
	v_lshlrev_b32_e32 v16, 4, v16
	v_lshlrev_b32_e32 v12, 4, v12
	v_add_f32_e32 v6, v6, v42
	v_add_f32_e32 v7, v7, v43
	v_lshlrev_b32_e32 v4, 4, v4
	v_add3_u32 v16, v69, v16, v68
	v_add3_u32 v12, v72, v12, v68
	v_max_f32_e32 v6, 0, v6
	v_max_f32_e32 v7, 0, v7
	v_add_f32_e32 v8, v8, v44
	v_add_f32_e32 v9, v9, v45
	v_add3_u32 v4, v73, v4, v68
	ds_write_b64 v16, v[14:15]
	ds_write_b64 v12, v[10:11]
	v_max_f32_e32 v8, 0, v8
	v_max_f32_e32 v9, 0, v9
	v_cvt_pk_bf16_f32 v6, v6, v7
	v_cvt_pk_bf16_f32 v7, v8, v9
	ds_write_b64 v16, v[6:7] offset:16384
	ds_write_b64 v4, v[2:3]
	v_and_b32_e32 v2, 0x1f0, v1
	v_mov_b32_e32 v3, 0
	v_lshl_add_u64 v[2:3], s[0:1], 0, v[2:3]
	s_mov_b64 s[0:1], 0x2000000
	v_ashrrev_i32_e32 v6, 5, v0
	v_lshl_add_u64 v[10:11], v[2:3], 0, s[0:1]
	v_xor_b32_e32 v2, v6, v0
	v_lshlrev_b32_e32 v2, 4, v2
	v_lshlrev_b32_e32 v1, 9, v6
	v_and_b32_e32 v2, 0x1f0, v2
	v_add3_u32 v1, 0, v1, v2
	s_waitcnt lgkmcnt(0)
	s_barrier
	ds_read_b128 v[2:5], v1
	v_ashrrev_i32_e32 v7, 31, v6
	v_add_u32_e32 v1, 0x200, v0
	v_lshlrev_b64 v[6:7], 11, v[6:7]
	v_ashrrev_i32_e32 v14, 5, v1
	v_lshl_add_u64 v[12:13], v[10:11], 0, v[6:7]
	v_xor_b32_e32 v6, v14, v0
	v_lshlrev_b32_e32 v6, 4, v6
	v_lshlrev_b32_e32 v1, 9, v14
	v_and_b32_e32 v6, 0x1f0, v6
	v_add3_u32 v1, 0, v1, v6
	ds_read_b128 v[6:9], v1
	v_ashrrev_i32_e32 v15, 31, v14
	s_waitcnt lgkmcnt(1)
	global_store_dwordx4 v[12:13], v[2:5], off sc1
	v_add_u32_e32 v1, 0x400, v0
	s_nop 0
	v_lshlrev_b64 v[2:3], 11, v[14:15]
	v_lshl_add_u64 v[2:3], v[10:11], 0, v[2:3]
	s_waitcnt lgkmcnt(0)
	global_store_dwordx4 v[2:3], v[6:9], off sc1
	s_nop 1
	v_ashrrev_i32_e32 v6, 5, v1
	v_xor_b32_e32 v2, v6, v0
	v_lshlrev_b32_e32 v2, 4, v2
	v_lshlrev_b32_e32 v1, 9, v6
	v_and_b32_e32 v2, 0x1f0, v2
	v_add3_u32 v1, 0, v1, v2
	ds_read_b128 v[2:5], v1
	v_ashrrev_i32_e32 v7, 31, v6
	v_add_u32_e32 v1, 0x600, v0
	v_lshlrev_b64 v[6:7], 11, v[6:7]
	v_ashrrev_i32_e32 v14, 5, v1
	v_lshl_add_u64 v[12:13], v[10:11], 0, v[6:7]
	v_xor_b32_e32 v6, v14, v0
	v_lshlrev_b32_e32 v6, 4, v6
	v_lshlrev_b32_e32 v1, 9, v14
	v_and_b32_e32 v6, 0x1f0, v6
	v_add3_u32 v1, 0, v1, v6
	ds_read_b128 v[6:9], v1
	v_ashrrev_i32_e32 v15, 31, v14
	s_waitcnt lgkmcnt(1)
	global_store_dwordx4 v[12:13], v[2:5], off sc1
	v_add_u32_e32 v1, 0x800, v0
	s_nop 0
	v_lshlrev_b64 v[2:3], 11, v[14:15]
	v_lshl_add_u64 v[2:3], v[10:11], 0, v[2:3]
	s_waitcnt lgkmcnt(0)
	global_store_dwordx4 v[2:3], v[6:9], off sc1
	s_nop 1
	v_ashrrev_i32_e32 v6, 5, v1
	v_xor_b32_e32 v2, v6, v0
	v_lshlrev_b32_e32 v2, 4, v2
	v_lshlrev_b32_e32 v1, 9, v6
	v_and_b32_e32 v2, 0x1f0, v2
	v_add3_u32 v1, 0, v1, v2
	ds_read_b128 v[2:5], v1
	v_ashrrev_i32_e32 v7, 31, v6
	v_add_u32_e32 v1, 0xa00, v0
	v_lshlrev_b64 v[6:7], 11, v[6:7]
	v_ashrrev_i32_e32 v14, 5, v1
	v_lshl_add_u64 v[12:13], v[10:11], 0, v[6:7]
	v_xor_b32_e32 v6, v14, v0
	v_lshlrev_b32_e32 v6, 4, v6
	v_lshlrev_b32_e32 v1, 9, v14
	v_and_b32_e32 v6, 0x1f0, v6
	v_add3_u32 v1, 0, v1, v6
	ds_read_b128 v[6:9], v1
	v_ashrrev_i32_e32 v15, 31, v14
	s_waitcnt lgkmcnt(1)
	global_store_dwordx4 v[12:13], v[2:5], off sc1
	v_add_u32_e32 v1, 0xc00, v0
	s_nop 0
	v_lshlrev_b64 v[2:3], 11, v[14:15]
	v_lshl_add_u64 v[2:3], v[10:11], 0, v[2:3]
	s_waitcnt lgkmcnt(0)
	global_store_dwordx4 v[2:3], v[6:9], off sc1
	s_nop 1
	v_ashrrev_i32_e32 v6, 5, v1
	v_xor_b32_e32 v2, v6, v0
	v_lshlrev_b32_e32 v2, 4, v2
	v_lshlrev_b32_e32 v1, 9, v6
	v_and_b32_e32 v2, 0x1f0, v2
	v_add3_u32 v1, 0, v1, v2
	ds_read_b128 v[2:5], v1
	v_add_u32_e32 v1, 0xe00, v0
	v_ashrrev_i32_e32 v14, 5, v1
	v_xor_b32_e32 v0, v14, v0
	v_lshlrev_b32_e32 v0, 4, v0
	v_ashrrev_i32_e32 v7, 31, v6
	v_lshlrev_b32_e32 v1, 9, v14
	v_and_b32_e32 v0, 0x1f0, v0
	v_lshlrev_b64 v[6:7], 11, v[6:7]
	v_add3_u32 v0, 0, v1, v0
	v_lshl_add_u64 v[12:13], v[10:11], 0, v[6:7]
	ds_read_b128 v[6:9], v0
	v_ashrrev_i32_e32 v15, 31, v14
	v_lshlrev_b64 v[0:1], 11, v[14:15]
	v_lshl_add_u64 v[0:1], v[10:11], 0, v[0:1]
	s_waitcnt lgkmcnt(1)
	global_store_dwordx4 v[12:13], v[2:5], off sc1
	s_waitcnt lgkmcnt(0)
	global_store_dwordx4 v[0:1], v[6:9], off sc1
	s_endpgm
.Lrot1_loop:
	s_and_b32 s0, s29, 0x10000
	v_add_u32_e32 v211, s0, v209
	v_add_u32_e32 v242, s0, v210
	s_xor_b32 s0, s0, 0x10000
	s_and_b32 s1, s22, 0x3c0
	s_add_i32 s23, s0, 0
	s_lshl_b32 s0, s1, 2
	s_add_u32 s20, s25, s0
	s_waitcnt vmcnt(10)
	v_cvt_pk_bf16_f32 v46, v46, v47
	v_cvt_pk_bf16_f32 v47, v48, v49
	v_cvt_pk_bf16_f32 v48, v42, v43
	v_cvt_pk_bf16_f32 v49, v44, v45
	s_waitcnt vmcnt(8)
	v_cvt_pk_bf16_f32 v38, v38, v39
	v_cvt_pk_bf16_f32 v39, v40, v41
	v_cvt_pk_bf16_f32 v40, v34, v35
	v_add_u32_e32 v34, s23, v208
	s_addc_u32 s21, s26, 0
	s_lshl_b32 s0, s1, 1
	v_cvt_pk_bf16_f32 v41, v36, v37
	v_lshlrev_b32_e32 v182, 2, v178
	v_add_u32_e32 v35, s23, v205
	v_add_u32_e32 v36, s23, v206
	v_add_u32_e32 v37, s23, v207
	ds_write_b128 v34, v[46:49]
	ds_write_b128 v35, v[38:41]
	s_waitcnt vmcnt(7)
	ds_write_b128 v36, v[30:33] offset:32768
	s_waitcnt vmcnt(6)
	ds_write_b128 v37, v[26:29] offset:32768
	v_lshl_add_u64 v[26:27], s[20:21], 0, v[180:181]
	v_lshl_add_u64 v[28:29], s[20:21], 0, v[184:185]
	s_add_u32 s0, s27, s0
	v_lshl_add_u64 v[26:27], v[26:27], 0, v[182:183]
	v_lshl_add_u64 v[28:29], v[28:29], 0, v[182:183]
	s_addc_u32 s1, s28, 0
	v_lshlrev_b32_e32 v240, 1, v178
	v_mov_b32_e32 v241, v183
	global_load_dwordx4 v[42:45], v[26:27], off offset:16
	global_load_dwordx4 v[46:49], v[26:27], off
	global_load_dwordx4 v[34:37], v[28:29], off offset:16
	global_load_dwordx4 v[38:41], v[28:29], off
	v_lshl_add_u64 v[26:27], s[0:1], 0, v[186:187]
	v_lshl_add_u64 v[28:29], s[0:1], 0, v[188:189]
	v_lshl_add_u64 v[26:27], v[26:27], 0, v[240:241]
	v_lshl_add_u64 v[28:29], v[28:29], 0, v[240:241]
	global_load_dwordx4 v[30:33], v[26:27], off
	s_nop 0
	global_load_dwordx4 v[26:29], v[28:29], off
	ds_read_b128 v[212:215], v242 offset:0
	ds_read_b128 v[216:219], v242 offset:0x800
	ds_read_b128 v[220:223], v242 offset:0x1000
	ds_read_b128 v[224:227], v242 offset:0x1800
	ds_read_b128 v[228:231], v211 offset:0
	ds_read_b128 v[232:235], v211 offset:0x800
	ds_read_b128 v[236:239], v211 offset:0x1000
	s_nop 0
	s_waitcnt lgkmcnt(2)
	s_nop 0
	v_mfma_f32_16x16x32_bf16 v[174:177], v[212:215], v[228:231], v[174:177]
	v_mfma_f32_16x16x32_bf16 v[170:173], v[216:219], v[228:231], v[170:173]
	v_mfma_f32_16x16x32_bf16 v[166:169], v[220:223], v[228:231], v[166:169]
	v_mfma_f32_16x16x32_bf16 v[162:165], v[224:227], v[228:231], v[162:165]
	ds_read_b128 v[228:231], v211 offset:0x1800
	s_waitcnt lgkmcnt(2)
	s_nop 0
	v_mfma_f32_16x16x32_bf16 v[158:161], v[212:215], v[232:235], v[158:161]
	v_mfma_f32_16x16x32_bf16 v[154:157], v[216:219], v[232:235], v[154:157]
	v_mfma_f32_16x16x32_bf16 v[150:153], v[220:223], v[232:235], v[150:153]
	v_mfma_f32_16x16x32_bf16 v[146:149], v[224:227], v[232:235], v[146:149]
	ds_read_b128 v[232:235], v211 offset:0x2000
	s_waitcnt lgkmcnt(2)
	s_nop 0
	v_mfma_f32_16x16x32_bf16 v[142:145], v[212:215], v[236:239], v[142:145]
	v_mfma_f32_16x16x32_bf16 v[138:141], v[216:219], v[236:239], v[138:141]
	v_mfma_f32_16x16x32_bf16 v[134:137], v[220:223], v[236:239], v[134:137]
	v_mfma_f32_16x16x32_bf16 v[130:133], v[224:227], v[236:239], v[130:133]
	ds_read_b128 v[236:239], v211 offset:0x2800
	s_waitcnt lgkmcnt(2)
	s_nop 0
	v_mfma_f32_16x16x32_bf16 v[126:129], v[212:215], v[228:231], v[126:129]
	v_mfma_f32_16x16x32_bf16 v[122:125], v[216:219], v[228:231], v[122:125]
	v_mfma_f32_16x16x32_bf16 v[118:121], v[220:223], v[228:231], v[118:121]
	v_mfma_f32_16x16x32_bf16 v[114:117], v[224:227], v[228:231], v[114:117]
	ds_read_b128 v[228:231], v211 offset:0x3000
	s_waitcnt lgkmcnt(2)
	s_nop 0
	v_mfma_f32_16x16x32_bf16 v[110:113], v[212:215], v[232:235], v[110:113]
	v_mfma_f32_16x16x32_bf16 v[106:109], v[216:219], v[232:235], v[106:109]
	v_mfma_f32_16x16x32_bf16 v[102:105], v[220:223], v[232:235], v[102:105]
	v_mfma_f32_16x16x32_bf16 v[98:101], v[224:227], v[232:235], v[98:101]
	ds_read_b128 v[232:235], v211 offset:0x3800
	s_waitcnt lgkmcnt(2)
	s_nop 0
	v_mfma_f32_16x16x32_bf16 v[94:97], v[212:215], v[236:239], v[94:97]
	v_mfma_f32_16x16x32_bf16 v[90:93], v[216:219], v[236:239], v[90:93]
	v_mfma_f32_16x16x32_bf16 v[86:89], v[220:223], v[236:239], v[86:89]
	v_mfma_f32_16x16x32_bf16 v[82:85], v[224:227], v[236:239], v[82:85]
	s_waitcnt lgkmcnt(1)
	s_nop 0
	v_mfma_f32_16x16x32_bf16 v[78:81], v[212:215], v[228:231], v[78:81]
	v_mfma_f32_16x16x32_bf16 v[74:77], v[216:219], v[228:231], v[74:77]
	v_mfma_f32_16x16x32_bf16 v[70:73], v[220:223], v[228:231], v[70:73]
	v_mfma_f32_16x16x32_bf16 v[66:69], v[224:227], v[228:231], v[66:69]
	s_waitcnt lgkmcnt(0)
	s_nop 0
	v_mfma_f32_16x16x32_bf16 v[62:65], v[212:215], v[232:235], v[62:65]
	v_mfma_f32_16x16x32_bf16 v[58:61], v[216:219], v[232:235], v[58:61]
	v_mfma_f32_16x16x32_bf16 v[54:57], v[220:223], v[232:235], v[54:57]
	v_mfma_f32_16x16x32_bf16 v[50:53], v[224:227], v[232:235], v[50:53]
	s_waitcnt vmcnt(10)
	v_cvt_pk_bf16_f32 v22, v22, v23
	v_cvt_pk_bf16_f32 v23, v24, v25
	v_cvt_pk_bf16_f32 v24, v6, v7
	v_cvt_pk_bf16_f32 v25, v8, v9
	v_add_u32_e32 v6, s23, v204
	s_waitcnt vmcnt(9)
	v_cvt_pk_bf16_f32 v8, v2, v3
	v_add_u32_e32 v2, s23, v201
	ds_write_b128 v6, v[22:25]
	s_waitcnt vmcnt(8)
	v_cvt_pk_bf16_f32 v6, v10, v11
	v_cvt_pk_bf16_f32 v7, v12, v13
	v_cvt_pk_bf16_f32 v9, v4, v5
	ds_write_b128 v2, v[6:9]
	v_add_u32_e32 v2, s23, v202
	s_waitcnt vmcnt(7)
	ds_write_b128 v2, v[18:21] offset:32768
	v_add_u32_e32 v2, s23, v203
	s_waitcnt vmcnt(6)
	ds_write_b128 v2, v[14:17] offset:32768
	v_lshl_add_u64 v[2:3], s[20:21], 0, v[190:191]
	v_lshl_add_u64 v[2:3], v[2:3], 0, v[182:183]
	global_load_dwordx4 v[6:9], v[2:3], off offset:16
	global_load_dwordx4 v[22:25], v[2:3], off
	v_lshl_add_u64 v[2:3], s[20:21], 0, v[192:193]
	v_lshl_add_u64 v[14:15], s[0:1], 0, v[194:195]
	v_lshl_add_u64 v[16:17], s[0:1], 0, v[196:197]
	v_lshl_add_u64 v[10:11], v[2:3], 0, v[182:183]
	v_lshl_add_u64 v[14:15], v[14:15], 0, v[240:241]
	v_lshl_add_u64 v[16:17], v[16:17], 0, v[240:241]
	global_load_dwordx4 v[2:5], v[10:11], off offset:16
	s_nop 0
	global_load_dwordx4 v[10:13], v[10:11], off
	s_nop 0
	global_load_dwordx4 v[18:21], v[14:15], off
	s_nop 0
	global_load_dwordx4 v[14:17], v[16:17], off
	ds_read_b128 v[212:215], v242 offset:0x400
	ds_read_b128 v[216:219], v242 offset:0xc00
	ds_read_b128 v[220:223], v242 offset:0x1400
	ds_read_b128 v[224:227], v242 offset:0x1c00
	ds_read_b128 v[228:231], v211 offset:0x400
	ds_read_b128 v[232:235], v211 offset:0xc00
	ds_read_b128 v[236:239], v211 offset:0x1400
	s_nop 0
	s_waitcnt lgkmcnt(2)
	s_nop 0
	v_mfma_f32_16x16x32_bf16 v[174:177], v[212:215], v[228:231], v[174:177]
	v_mfma_f32_16x16x32_bf16 v[170:173], v[216:219], v[228:231], v[170:173]
	v_mfma_f32_16x16x32_bf16 v[166:169], v[220:223], v[228:231], v[166:169]
	v_mfma_f32_16x16x32_bf16 v[162:165], v[224:227], v[228:231], v[162:165]
	ds_read_b128 v[228:231], v211 offset:0x1c00
	s_waitcnt lgkmcnt(2)
	s_nop 0
	v_mfma_f32_16x16x32_bf16 v[158:161], v[212:215], v[232:235], v[158:161]
	v_mfma_f32_16x16x32_bf16 v[154:157], v[216:219], v[232:235], v[154:157]
	v_mfma_f32_16x16x32_bf16 v[150:153], v[220:223], v[232:235], v[150:153]
	v_mfma_f32_16x16x32_bf16 v[146:149], v[224:227], v[232:235], v[146:149]
	ds_read_b128 v[232:235], v211 offset:0x2400
	s_waitcnt lgkmcnt(2)
	s_nop 0
	v_mfma_f32_16x16x32_bf16 v[142:145], v[212:215], v[236:239], v[142:145]
	v_mfma_f32_16x16x32_bf16 v[138:141], v[216:219], v[236:239], v[138:141]
	v_mfma_f32_16x16x32_bf16 v[134:137], v[220:223], v[236:239], v[134:137]
	v_mfma_f32_16x16x32_bf16 v[130:133], v[224:227], v[236:239], v[130:133]
	ds_read_b128 v[236:239], v211 offset:0x2c00
	s_waitcnt lgkmcnt(2)
	s_nop 0
	v_mfma_f32_16x16x32_bf16 v[126:129], v[212:215], v[228:231], v[126:129]
	v_mfma_f32_16x16x32_bf16 v[122:125], v[216:219], v[228:231], v[122:125]
	v_mfma_f32_16x16x32_bf16 v[118:121], v[220:223], v[228:231], v[118:121]
	v_mfma_f32_16x16x32_bf16 v[114:117], v[224:227], v[228:231], v[114:117]
	ds_read_b128 v[228:231], v211 offset:0x3400
	s_waitcnt lgkmcnt(2)
	s_nop 0
	v_mfma_f32_16x16x32_bf16 v[110:113], v[212:215], v[232:235], v[110:113]
	v_mfma_f32_16x16x32_bf16 v[106:109], v[216:219], v[232:235], v[106:109]
	v_mfma_f32_16x16x32_bf16 v[102:105], v[220:223], v[232:235], v[102:105]
	v_mfma_f32_16x16x32_bf16 v[98:101], v[224:227], v[232:235], v[98:101]
	ds_read_b128 v[232:235], v211 offset:0x3c00
	s_waitcnt lgkmcnt(2)
	s_nop 0
	v_mfma_f32_16x16x32_bf16 v[94:97], v[212:215], v[236:239], v[94:97]
	v_mfma_f32_16x16x32_bf16 v[90:93], v[216:219], v[236:239], v[90:93]
	v_mfma_f32_16x16x32_bf16 v[86:89], v[220:223], v[236:239], v[86:89]
	v_mfma_f32_16x16x32_bf16 v[82:85], v[224:227], v[236:239], v[82:85]
	s_waitcnt lgkmcnt(1)
	s_nop 0
	v_mfma_f32_16x16x32_bf16 v[78:81], v[212:215], v[228:231], v[78:81]
	v_mfma_f32_16x16x32_bf16 v[74:77], v[216:219], v[228:231], v[74:77]
	v_mfma_f32_16x16x32_bf16 v[70:73], v[220:223], v[228:231], v[70:73]
	v_mfma_f32_16x16x32_bf16 v[66:69], v[224:227], v[228:231], v[66:69]
	s_waitcnt lgkmcnt(0)
	s_nop 0
	v_mfma_f32_16x16x32_bf16 v[62:65], v[212:215], v[232:235], v[62:65]
	v_mfma_f32_16x16x32_bf16 v[58:61], v[216:219], v[232:235], v[58:61]
	v_mfma_f32_16x16x32_bf16 v[54:57], v[220:223], v[232:235], v[54:57]
	v_mfma_f32_16x16x32_bf16 v[50:53], v[224:227], v[232:235], v[50:53]
	s_waitcnt lgkmcnt(0)
	s_add_i32 s22, s22, 64
	s_add_i32 s29, s29, 0x10000
	s_cmp_lg_u32 s29, 0xe0000
	s_barrier
	s_cbranch_scc1 .Lrot1_loop
	s_branch .Lrot1_done
.Lrot2_loop:
	s_and_b32 s0, s3, 0x10000
	v_add_u32_e32 v158, s0, v128
	v_add_u32_e32 v159, s0, v129
	s_xor_b32 s0, s0, 0x10000
	s_and_b32 s6, s2, 0x3c0
	s_add_i32 s14, s0, 0
	s_lshl_b32 s0, s6, 2
	s_lshl_b32 s6, s6, 1
	s_add_u32 s6, s12, s6
	s_waitcnt vmcnt(6)
	v_cvt_pk_bf16_f32 v34, v34, v35
	v_cvt_pk_bf16_f32 v35, v36, v37
	v_cvt_pk_bf16_f32 v36, v30, v31
	v_cvt_pk_bf16_f32 v37, v32, v33
	v_add_u32_e32 v30, s14, v125
	s_addc_u32 s7, s13, 0
	v_add_u32_e32 v31, s14, v126
	v_add_u32_e32 v32, s14, v127
	ds_write_b128 v30, v[34:37]
	s_waitcnt vmcnt(5)
	ds_write_b128 v31, v[26:29] offset:32768
	s_waitcnt vmcnt(4)
	ds_write_b128 v32, v[22:25] offset:32768
	v_lshl_add_u64 v[22:23], s[6:7], 0, v[102:103]
	v_lshl_add_u64 v[24:25], s[6:7], 0, v[104:105]
	v_lshl_add_u64 v[130:131], v[114:115], 0, s[0:1]
	v_lshl_add_u64 v[22:23], v[98:99], 1, v[22:23]
	v_lshl_add_u64 v[24:25], v[100:101], 1, v[24:25]
	global_load_dwordx4 v[30:33], v[130:131], off offset:16
	global_load_dwordx4 v[34:37], v[130:131], off
	global_load_dwordx4 v[26:29], v[22:23], off
	s_nop 0
	global_load_dwordx4 v[22:25], v[24:25], off
	ds_read_b128 v[130:133], v159 offset:0
	ds_read_b128 v[134:137], v159 offset:0x800
	ds_read_b128 v[138:141], v159 offset:0x1000
	ds_read_b128 v[142:145], v159 offset:0x1800
	ds_read_b128 v[146:149], v158 offset:0
	ds_read_b128 v[150:153], v158 offset:0x800
	ds_read_b128 v[154:157], v158 offset:0x1000
	s_nop 0
	s_waitcnt lgkmcnt(2)
	s_nop 0
	v_mfma_f32_16x16x32_bf16 v[94:97], v[130:133], v[146:149], v[94:97]
	v_mfma_f32_16x16x32_bf16 v[90:93], v[134:137], v[146:149], v[90:93]
	v_mfma_f32_16x16x32_bf16 v[86:89], v[138:141], v[146:149], v[86:89]
	v_mfma_f32_16x16x32_bf16 v[82:85], v[142:145], v[146:149], v[82:85]
	ds_read_b128 v[146:149], v158 offset:0x1800
	s_waitcnt lgkmcnt(2)
	s_nop 0
	v_mfma_f32_16x16x32_bf16 v[78:81], v[130:133], v[150:153], v[78:81]
	v_mfma_f32_16x16x32_bf16 v[74:77], v[134:137], v[150:153], v[74:77]
	v_mfma_f32_16x16x32_bf16 v[70:73], v[138:141], v[150:153], v[70:73]
	v_mfma_f32_16x16x32_bf16 v[66:69], v[142:145], v[150:153], v[66:69]
	s_waitcnt lgkmcnt(1)
	s_nop 0
	v_mfma_f32_16x16x32_bf16 v[62:65], v[130:133], v[154:157], v[62:65]
	v_mfma_f32_16x16x32_bf16 v[58:61], v[134:137], v[154:157], v[58:61]
	v_mfma_f32_16x16x32_bf16 v[54:57], v[138:141], v[154:157], v[54:57]
	v_mfma_f32_16x16x32_bf16 v[50:53], v[142:145], v[154:157], v[50:53]
	s_waitcnt lgkmcnt(0)
	s_nop 0
	v_mfma_f32_16x16x32_bf16 v[46:49], v[130:133], v[146:149], v[46:49]
	v_mfma_f32_16x16x32_bf16 v[42:45], v[134:137], v[146:149], v[42:45]
	v_mfma_f32_16x16x32_bf16 v[38:41], v[138:141], v[146:149], v[38:41]
	v_mfma_f32_16x16x32_bf16 v[2:5], v[142:145], v[146:149], v[2:5]
	v_add_u32_e32 v130, s14, v122
	s_waitcnt vmcnt(6)
	v_cvt_pk_bf16_f32 v10, v10, v11
	v_cvt_pk_bf16_f32 v11, v12, v13
	v_cvt_pk_bf16_f32 v12, v6, v7
	v_add_u32_e32 v6, s14, v123
	v_cvt_pk_bf16_f32 v13, v8, v9
	ds_write_b128 v130, v[10:13]
	s_waitcnt vmcnt(5)
	ds_write_b128 v6, v[18:21] offset:32768
	v_add_u32_e32 v6, s14, v124
	s_waitcnt vmcnt(4)
	ds_write_b128 v6, v[14:17] offset:32768
	v_lshl_add_u64 v[14:15], s[6:7], 0, v[110:111]
	v_lshl_add_u64 v[16:17], s[6:7], 0, v[112:113]
	v_lshl_add_u64 v[10:11], v[116:117], 0, s[0:1]
	v_lshl_add_u64 v[14:15], v[106:107], 1, v[14:15]
	v_lshl_add_u64 v[16:17], v[108:109], 1, v[16:17]
	global_load_dwordx4 v[6:9], v[10:11], off offset:16
	s_nop 0
	global_load_dwordx4 v[10:13], v[10:11], off
	s_nop 0
	global_load_dwordx4 v[18:21], v[14:15], off
	s_nop 0
	global_load_dwordx4 v[14:17], v[16:17], off
	ds_read_b128 v[130:133], v159 offset:0x400
	ds_read_b128 v[134:137], v159 offset:0xc00
	ds_read_b128 v[138:141], v159 offset:0x1400
	ds_read_b128 v[142:145], v159 offset:0x1c00
	ds_read_b128 v[146:149], v158 offset:0x400
	ds_read_b128 v[150:153], v158 offset:0xc00
	ds_read_b128 v[154:157], v158 offset:0x1400
	s_nop 0
	s_waitcnt lgkmcnt(2)
	s_nop 0
	v_mfma_f32_16x16x32_bf16 v[94:97], v[130:133], v[146:149], v[94:97]
	v_mfma_f32_16x16x32_bf16 v[90:93], v[134:137], v[146:149], v[90:93]
	v_mfma_f32_16x16x32_bf16 v[86:89], v[138:141], v[146:149], v[86:89]
	v_mfma_f32_16x16x32_bf16 v[82:85], v[142:145], v[146:149], v[82:85]
	ds_read_b128 v[146:149], v158 offset:0x1c00
	s_waitcnt lgkmcnt(2)
	s_nop 0
	v_mfma_f32_16x16x32_bf16 v[78:81], v[130:133], v[150:153], v[78:81]
	v_mfma_f32_16x16x32_bf16 v[74:77], v[134:137], v[150:153], v[74:77]
	v_mfma_f32_16x16x32_bf16 v[70:73], v[138:141], v[150:153], v[70:73]
	v_mfma_f32_16x16x32_bf16 v[66:69], v[142:145], v[150:153], v[66:69]
	s_waitcnt lgkmcnt(1)
	s_nop 0
	v_mfma_f32_16x16x32_bf16 v[62:65], v[130:133], v[154:157], v[62:65]
	v_mfma_f32_16x16x32_bf16 v[58:61], v[134:137], v[154:157], v[58:61]
	v_mfma_f32_16x16x32_bf16 v[54:57], v[138:141], v[154:157], v[54:57]
	v_mfma_f32_16x16x32_bf16 v[50:53], v[142:145], v[154:157], v[50:53]
	s_waitcnt lgkmcnt(0)
	s_nop 0
	v_mfma_f32_16x16x32_bf16 v[46:49], v[130:133], v[146:149], v[46:49]
	v_mfma_f32_16x16x32_bf16 v[42:45], v[134:137], v[146:149], v[42:45]
	v_mfma_f32_16x16x32_bf16 v[38:41], v[138:141], v[146:149], v[38:41]
	v_mfma_f32_16x16x32_bf16 v[2:5], v[142:145], v[146:149], v[2:5]
	s_waitcnt lgkmcnt(0)
	s_add_i32 s2, s2, 64
	s_add_i32 s3, s3, 0x10000
	s_cmp_lg_u32 s3, 0xe0000
	s_barrier
	s_cbranch_scc1 .Lrot2_loop
	s_branch .Lrot2_done

	.amdhsa_kernel _Z9proj_gemmPKfS0_S0_PK14__hip_bfloat16S0_S0_S0_PS1_
		.amdhsa_group_segment_fixed_size 0
		.amdhsa_private_segment_fixed_size 0
		.amdhsa_kernarg_size 64
		.amdhsa_user_sgpr_count 2
		.amdhsa_user_sgpr_dispatch_ptr 0
		.amdhsa_user_sgpr_queue_ptr 0
		.amdhsa_user_sgpr_kernarg_segment_ptr 1
		.amdhsa_user_sgpr_dispatch_id 0
		.amdhsa_user_sgpr_kernarg_preload_length 0
		.amdhsa_user_sgpr_kernarg_preload_offset 0
		.amdhsa_user_sgpr_private_segment_size 0
		.amdhsa_uses_dynamic_stack 0
		.amdhsa_enable_private_segment 0
		.amdhsa_system_sgpr_workgroup_id_x 1
		.amdhsa_system_sgpr_workgroup_id_y 0
		.amdhsa_system_sgpr_workgroup_id_z 0
		.amdhsa_system_sgpr_workgroup_info 0
		.amdhsa_system_vgpr_workitem_id 0
		.amdhsa_next_free_vgpr 243
		.amdhsa_next_free_sgpr 41
		.amdhsa_accum_offset 244
		.amdhsa_reserve_vcc 0
		.amdhsa_float_round_mode_32 0
		.amdhsa_float_round_mode_16_64 0
		.amdhsa_float_denorm_mode_32 3
		.amdhsa_float_denorm_mode_16_64 3
		.amdhsa_dx10_clamp 1
		.amdhsa_ieee_mode 1
		.amdhsa_fp16_overflow 0
		.amdhsa_tg_split 0
		.amdhsa_exception_fp_ieee_invalid_op 0
		.amdhsa_exception_fp_denorm_src 0
		.amdhsa_exception_fp_ieee_div_zero 0
		.amdhsa_exception_fp_ieee_overflow 0
		.amdhsa_exception_fp_ieee_underflow 0
		.amdhsa_exception_fp_ieee_inexact 0
		.amdhsa_exception_int_div_zero 0
	.end_amdhsa_kernel
